# stack7 + retA staging: all 24 global loads per retA_unit2 call hoisted into fresh VGPRs and issued together (call 2 loads issued during call 1 compute)
# speedup vs baseline: 1.0065x; 1.0065x over previous
; #define GAS __attribute__((address_space(1)))
; template <int MODE  > __device__ __forceinline__ void ret_stage_rot(LAS unsigned char* tile, const bf16* src  , const f32x2* rot  , float sc, float l2g, int tid) {
; #pragma unroll
;     for (int i = 0; i < 2; ++i) { const int item = tid + 512 * i, j = item >> 3, cc = item & 7;
;         const v4u lo = *(const GAS v4u*)(src + (size_t)j * LDP + 8 * cc), hh = *(const GAS v4u*)(src + (size_t)j * LDP + 64 + 8 * cc);
;         const GAS f32x4* rp = (const GAS f32x4*)(rot + (size_t)j * 64 + 8 * cc);
;         const f32x4 c0 = rp[0], c1 = rp[1], c2 = rp[2], c3 = rp[3];
;         const float cs[8] = {c0.x, c0.z, c1.x, c1.z, c2.x, c2.z, c3.x, c3.z}, sn[8] = {c0.y, c0.w, c1.y, c1.w, c2.y, c2.w, c3.y, c3.w};
;         const float a[8] = {bflo(lo.x), bfhi(lo.x), bflo(lo.y), bfhi(lo.y), bflo(lo.z), bfhi(lo.z), bflo(lo.w), bfhi(lo.w)};
;         const float bb[8] = {bflo(hh.x), bfhi(hh.x), bflo(hh.y), bfhi(hh.y), bflo(hh.z), bfhi(hh.z), bflo(hh.w), bfhi(hh.w)};
;         const float s = MODE == 1 ? sc * __builtin_amdgcn_exp2f((float)(127 - j) * l2g) : sc;
;         float o1[8], o2[8];
; #pragma unroll
;         for (int e = 0; e < 8; ++e) { o1[e] = (a[e] * cs[e] - bb[e] * sn[e]) * s; o2[e] = (bb[e] * cs[e] + a[e] * sn[e]) * s; }
;         v4u w; w.x = pk2(o1[0], o1[1]); w.y = pk2(o1[2], o1[3]); w.z = pk2(o1[4], o1[5]); w.w = pk2(o1[6], o1[7]); *(LAS v4u*)(tile + offb(j, cc)) = w;
;         w.x = pk2(o2[0], o2[1]); w.y = pk2(o2[2], o2[3]); w.z = pk2(o2[4], o2[5]); w.w = pk2(o2[6], o2[7]); *(LAS v4u*)(tile + offb(j, cc + 8)) = w; }
; }
; __device__ __forceinline__ void ret_stage_plain(LAS unsigned char* tile, const bf16* src, int ld, int tid) {
; #pragma unroll
;     for (int i = 0; i < 4; ++i) { const int item = tid + 512 * i, row = item >> 4, ch = item & 15; *(LAS v4u*)(tile + offb(row, ch)) = *(const GAS v4u*)(src + (size_t)row * ld + 8 * ch); }
; __device__ __forceinline__ void retA_unit2(LAS unsigned char* lds, const bf16* proj, const f32x2* rot, float* KV, int uA, int uB, int tid, int lane, int wid) {
;     asm volatile("" : "+v"(tid)); lane = tid & 63;
;     const int hi = lane >> 5, r32 = lane & 31;
; #pragma unroll
;     for (int s = 0; s < 2; ++s) { const int u = s ? uB : uA; const int bh = u >> 5, c = u & 31, b = bh >> 3, h = bh & 7; const size_t t0 = (size_t)b * SEQ + c * 128;
.LBB0_339:
	s_andn2_b64 vcc, exec, s[36:37]
	s_cbranch_vccnz .LBB0_341
	v_mov_b32_e32 v68, v1
	v_readlane_b32 s4, v252, 24
	v_ashrrev_i32_e32 v36, 3, v68
	s_waitcnt vmcnt(0) lgkmcnt(0)
	v_sub_u32_e32 v4, 0x7f, v36
	v_cvt_f32_i32_e32 v61, v4
	v_lshlrev_b32_e32 v4, 2, v36
	v_and_b32_e32 v10, 7, v68
	v_and_b32_e32 v4, 12, v4
	v_bfe_u32 v5, v36, 2, 2
	v_bitop3_b32 v8, v4, v10, v5 bitop3:0x36
	v_lshlrev_b32_e32 v60, 4, v8
	v_add_u32_e32 v8, 0x200, v68
	v_ashrrev_i32_e32 v34, 3, v8
	v_sub_u32_e32 v9, 0x7f, v34
	v_cvt_f32_i32_e32 v57, v9
	v_lshlrev_b32_e32 v9, 2, v34
	v_or_b32_e32 v2, 8, v10
	v_and_b32_e32 v9, 12, v9
	v_bfe_u32 v11, v34, 2, 2
	v_bitop3_b32 v4, v4, v2, v5 bitop3:0x36
	v_bitop3_b32 v2, v9, v2, v11 bitop3:0x36
	v_ashrrev_i32_e32 v52, 4, v68
	v_lshlrev_b32_e32 v55, 4, v2
	v_lshlrev_b32_e32 v2, 2, v52
	v_bitop3_b32 v12, v9, v10, v11 bitop3:0x36
	v_and_b32_e32 v69, 15, v68
	v_and_b32_e32 v2, 12, v2
	v_bfe_u32 v9, v52, 2, 2
	v_bitop3_b32 v2, v2, v69, v9 bitop3:0x36
	v_ashrrev_i32_e32 v49, 4, v8
	v_lshlrev_b32_e32 v53, 4, v2
	v_lshlrev_b32_e32 v2, 2, v49
	v_and_b32_e32 v2, 12, v2
	v_bfe_u32 v8, v49, 2, 2
	v_bitop3_b32 v2, v2, v69, v8 bitop3:0x36
	v_lshlrev_b32_e32 v50, 4, v2
	v_add_u32_e32 v2, 0x400, v68
	v_ashrrev_i32_e32 v46, 4, v2
	v_lshlrev_b32_e32 v2, 2, v46
	v_and_b32_e32 v2, 12, v2
	v_bfe_u32 v8, v46, 2, 2
	v_bitop3_b32 v2, v2, v69, v8 bitop3:0x36
	v_lshlrev_b32_e32 v48, 4, v2
	v_add_u32_e32 v2, 0x600, v68
	v_ashrrev_i32_e32 v44, 4, v2
	v_lshlrev_b32_e32 v2, 2, v44
	v_readlane_b32 s5, v252, 25
	v_and_b32_e32 v2, 12, v2
	v_bfe_u32 v8, v44, 2, 2
	s_load_dword s0, s[4:5], 0x0
	v_readlane_b32 s4, v252, 22
	v_ashrrev_i32_e32 v37, 31, v36
	v_bitop3_b32 v2, v2, v69, v8 bitop3:0x36
	v_readlane_b32 s24, v252, 28
	v_readlane_b32 s5, v252, 23
	v_lshlrev_b64 v[6:7], 9, v[36:37]
	v_lshlrev_b32_e32 v37, 4, v2
	v_lshlrev_b32_e32 v2, 6, v10
	v_readlane_b32 s25, v252, 29
	v_mov_b64_e32 v[42:43], s[4:5]
	v_mad_i64_i32 v[8:9], s[4:5], v36, s33, v[42:43]
	v_lshl_add_u64 v[16:17], s[24:25], 0, v[2:3]
	v_lshlrev_b32_e32 v2, 4, v10
	v_lshlrev_b32_e32 v56, 4, v12
	v_lshl_add_u64 v[12:13], v[8:9], 0, v[2:3]
	v_lshl_add_u64 v[6:7], v[16:17], 0, v[6:7]
	global_load_dwordx4 v[86:89], v[12:13], off
	global_load_dwordx4 v[90:93], v[12:13], off offset:128
	global_load_dwordx4 v[94:97], v[6:7], off offset:48
	global_load_dwordx4 v[98:101], v[6:7], off offset:32
	global_load_dwordx4 v[102:105], v[6:7], off offset:16
	global_load_dwordx4 v[106:109], v[6:7], off
	v_mad_i64_i32 v[202:203], s[100:101], v34, s33, v[42:43]
	v_lshl_add_u64 v[204:205], v[202:203], 0, v[2:3]
	global_load_dwordx4 v[110:113], v[204:205], off
	v_mad_i64_i32 v[202:203], s[100:101], v34, s33, v[42:43]
	v_lshl_add_u64 v[204:205], v[202:203], 0, v[2:3]
	global_load_dwordx4 v[114:117], v[204:205], off offset:128
	v_ashrrev_i32_e32 v202, 31, v34
	v_mov_b32_e32 v204, v34
	v_mov_b32_e32 v205, v202
	v_lshlrev_b64 v[206:207], 9, v[204:205]
	v_lshl_add_u64 v[208:209], v[16:17], 0, v[206:207]
	global_load_dwordx4 v[118:121], v[208:209], off offset:48
	v_ashrrev_i32_e32 v202, 31, v34
	v_mov_b32_e32 v204, v34
	v_mov_b32_e32 v205, v202
	v_lshlrev_b64 v[206:207], 9, v[204:205]
	v_lshl_add_u64 v[208:209], v[16:17], 0, v[206:207]
	global_load_dwordx4 v[122:125], v[208:209], off offset:32
	v_ashrrev_i32_e32 v202, 31, v34
	v_mov_b32_e32 v204, v34
	v_mov_b32_e32 v205, v202
	v_lshlrev_b64 v[206:207], 9, v[204:205]
	v_lshl_add_u64 v[208:209], v[16:17], 0, v[206:207]
	global_load_dwordx4 v[126:129], v[208:209], off offset:16
	v_ashrrev_i32_e32 v202, 31, v34
	v_mov_b32_e32 v204, v34
	v_mov_b32_e32 v205, v202
	v_lshlrev_b64 v[206:207], 9, v[204:205]
	v_lshl_add_u64 v[208:209], v[16:17], 0, v[206:207]
	global_load_dwordx4 v[130:133], v[208:209], off
	v_readlane_b32 s100, v252, 30
	v_readlane_b32 s101, v252, 31
	v_lshlrev_b32_e32 v202, 4, v69
	v_mov_b32_e32 v203, v3
	v_lshl_add_u64 v[204:205], s[100:101], 0, v[202:203]
	v_mad_i64_i32 v[206:207], s[100:101], v52, s33, v[204:205]
	global_load_dwordx4 v[134:137], v[206:207], off
	v_readlane_b32 s100, v252, 30
	v_readlane_b32 s101, v252, 31
	v_lshlrev_b32_e32 v202, 4, v69
	v_mov_b32_e32 v203, v3
	v_lshl_add_u64 v[204:205], s[100:101], 0, v[202:203]
	v_mad_i64_i32 v[206:207], s[100:101], v49, s33, v[204:205]
	global_load_dwordx4 v[138:141], v[206:207], off
	v_readlane_b32 s100, v252, 30
	v_readlane_b32 s101, v252, 31
	v_lshlrev_b32_e32 v202, 4, v69
	v_mov_b32_e32 v203, v3
	v_lshl_add_u64 v[204:205], s[100:101], 0, v[202:203]
	v_mad_i64_i32 v[206:207], s[100:101], v46, s33, v[204:205]
	global_load_dwordx4 v[142:145], v[206:207], off
	v_readlane_b32 s100, v252, 30
	v_readlane_b32 s101, v252, 31
	v_lshlrev_b32_e32 v202, 4, v69
	v_mov_b32_e32 v203, v3
	v_lshl_add_u64 v[204:205], s[100:101], 0, v[202:203]
	v_mad_i64_i32 v[206:207], s[100:101], v44, s33, v[204:205]
	global_load_dwordx4 v[146:149], v[206:207], off
	v_readlane_b32 s100, v252, 32
	v_readlane_b32 s101, v252, 33
	s_nop 1
	v_mov_b64_e32 v[202:203], s[100:101]
	v_mad_i64_i32 v[204:205], s[100:101], v36, s33, v[202:203]
	v_lshl_add_u64 v[206:207], v[204:205], 0, v[2:3]
	global_load_dwordx4 v[150:153], v[206:207], off
	v_readlane_b32 s100, v252, 32
	v_readlane_b32 s101, v252, 33
	s_nop 1
	v_mov_b64_e32 v[202:203], s[100:101]
	v_mad_i64_i32 v[204:205], s[100:101], v36, s33, v[202:203]
	v_lshl_add_u64 v[206:207], v[204:205], 0, v[2:3]
	global_load_dwordx4 v[154:157], v[206:207], off offset:128
	v_readlane_b32 s100, v252, 32
	v_readlane_b32 s101, v252, 33
	s_nop 1
	v_mov_b64_e32 v[202:203], s[100:101]
	v_mad_i64_i32 v[204:205], s[100:101], v34, s33, v[202:203]
	v_lshl_add_u64 v[206:207], v[204:205], 0, v[2:3]
; #define GAS __attribute__((address_space(1)))
; #define LAS __attribute__((address_space(3)))
; __device__ __forceinline__ unsigned pk2(float lo, float hi) { f32x2_t_ v = {lo, hi}; bf16x2_t_ b = __builtin_convertvector(v, bf16x2_t_); return __builtin_bit_cast(unsigned, b); }
; template <int MODE  > __device__ __forceinline__ void ret_stage_rot(LAS unsigned char* tile, const bf16* src  , const f32x2* rot  , float sc, float l2g, int tid) {
; #pragma unroll
;     for (int i = 0; i < 2; ++i) { const int item = tid + 512 * i, j = item >> 3, cc = item & 7;
;         const v4u lo = *(const GAS v4u*)(src + (size_t)j * LDP + 8 * cc), hh = *(const GAS v4u*)(src + (size_t)j * LDP + 64 + 8 * cc);
;         const GAS f32x4* rp = (const GAS f32x4*)(rot + (size_t)j * 64 + 8 * cc);
;         const f32x4 c0 = rp[0], c1 = rp[1], c2 = rp[2], c3 = rp[3];
;         const float cs[8] = {c0.x, c0.z, c1.x, c1.z, c2.x, c2.z, c3.x, c3.z}, sn[8] = {c0.y, c0.w, c1.y, c1.w, c2.y, c2.w, c3.y, c3.w};
;         const float a[8] = {bflo(lo.x), bfhi(lo.x), bflo(lo.y), bfhi(lo.y), bflo(lo.z), bfhi(lo.z), bflo(lo.w), bfhi(lo.w)};
;         const float bb[8] = {bflo(hh.x), bfhi(hh.x), bflo(hh.y), bfhi(hh.y), bflo(hh.z), bfhi(hh.z), bflo(hh.w), bfhi(hh.w)};
;         const float s = MODE == 1 ? sc * __builtin_amdgcn_exp2f((float)(127 - j) * l2g) : sc;
;         float o1[8], o2[8];
; #pragma unroll
;         for (int e = 0; e < 8; ++e) { o1[e] = (a[e] * cs[e] - bb[e] * sn[e]) * s; o2[e] = (bb[e] * cs[e] + a[e] * sn[e]) * s; }
;         v4u w; w.x = pk2(o1[0], o1[1]); w.y = pk2(o1[2], o1[3]); w.z = pk2(o1[4], o1[5]); w.w = pk2(o1[6], o1[7]); *(LAS v4u*)(tile + offb(j, cc)) = w;
;         w.x = pk2(o2[0], o2[1]); w.y = pk2(o2[2], o2[3]); w.z = pk2(o2[4], o2[5]); w.w = pk2(o2[6], o2[7]); *(LAS v4u*)(tile + offb(j, cc + 8)) = w; }
; }
; __device__ __forceinline__ void ret_stage_plain(LAS unsigned char* tile, const bf16* src, int ld, int tid) {
; #pragma unroll
;     for (int i = 0; i < 4; ++i) { const int item = tid + 512 * i, row = item >> 4, ch = item & 15; *(LAS v4u*)(tile + offb(row, ch)) = *(const GAS v4u*)(src + (size_t)row * ld + 8 * ch); }
	global_load_dwordx4 v[158:161], v[206:207], off
	v_readlane_b32 s100, v252, 32
	v_readlane_b32 s101, v252, 33
	s_nop 1
	v_mov_b64_e32 v[202:203], s[100:101]
	v_mad_i64_i32 v[204:205], s[100:101], v34, s33, v[202:203]
	v_lshl_add_u64 v[206:207], v[204:205], 0, v[2:3]
	global_load_dwordx4 v[162:165], v[206:207], off offset:128
	v_lshlrev_b32_e32 v202, 4, v69
	v_mov_b32_e32 v203, v3
	v_readlane_b32 s100, v252, 36
	v_readlane_b32 s101, v252, 37
	s_nop 1
	v_lshl_add_u64 v[204:205], s[100:101], 0, v[202:203]
	v_mad_i64_i32 v[206:207], s[100:101], v52, s33, v[204:205]
	global_load_dwordx4 v[166:169], v[206:207], off
	v_lshlrev_b32_e32 v202, 4, v69
	v_mov_b32_e32 v203, v3
	v_readlane_b32 s100, v252, 36
	v_readlane_b32 s101, v252, 37
	s_nop 1
	v_lshl_add_u64 v[204:205], s[100:101], 0, v[202:203]
	v_mad_i64_i32 v[206:207], s[100:101], v49, s33, v[204:205]
	global_load_dwordx4 v[170:173], v[206:207], off
	v_lshlrev_b32_e32 v202, 4, v69
	v_mov_b32_e32 v203, v3
	v_readlane_b32 s100, v252, 36
	v_readlane_b32 s101, v252, 37
	s_nop 1
	v_lshl_add_u64 v[204:205], s[100:101], 0, v[202:203]
	v_mad_i64_i32 v[206:207], s[100:101], v46, s33, v[204:205]
	global_load_dwordx4 v[174:177], v[206:207], off
	v_lshlrev_b32_e32 v202, 4, v69
	v_mov_b32_e32 v203, v3
	v_readlane_b32 s100, v252, 36
	v_readlane_b32 s101, v252, 37
	s_nop 1
	v_lshl_add_u64 v[204:205], s[100:101], 0, v[202:203]
	v_mad_i64_i32 v[206:207], s[100:101], v44, s33, v[204:205]
	global_load_dwordx4 v[178:181], v[206:207], off
	s_nop 0
	s_nop 0
	s_waitcnt lgkmcnt(0)
	v_mul_f32_e32 v6, s0, v61
	v_exp_f32_e32 v6, v6
	v_lshlrev_b32_e32 v58, 8, v36
	v_lshlrev_b32_e32 v59, 4, v4
	v_ashrrev_i32_e32 v35, 31, v34
	v_mul_f32_e32 v6, 0x3db504f3, v6
	v_lshlrev_b64 v[4:5], 9, v[34:35]
	v_lshl_add_u64 v[16:17], v[16:17], 0, v[4:5]
	v_lshlrev_b32_e32 v54, 8, v34
	v_lshlrev_b32_e32 v51, 8, v52
	v_lshlrev_b32_e32 v47, 8, v49
	v_lshlrev_b32_e32 v45, 8, v46
	v_lshlrev_b32_e32 v35, 8, v44
	v_readlane_b32 s18, v252, 32
	v_readlane_b32 s19, v252, 33
	v_readlane_b32 s3, v252, 19
	s_waitcnt vmcnt(23)
	v_lshlrev_b32_e32 v40, 16, v86
	s_waitcnt vmcnt(22)
	v_lshlrev_b32_e32 v62, 16, v90
	v_and_b32_e32 v63, 0xffff0000, v90
	s_waitcnt vmcnt(18)
	v_mov_b32_e32 v39, v108
	v_mov_b32_e32 v32, v107
	v_and_b32_e32 v41, 0xffff0000, v86
	v_mov_b32_e32 v38, v106
	v_mov_b32_e32 v33, v109
	v_pk_mul_f32 v[30:31], v[32:33], v[62:63]
	v_lshlrev_b32_e32 v12, 16, v91
	v_pk_fma_f32 v[30:31], v[38:39], v[40:41], v[30:31] neg_lo:[0,0,1] neg_hi:[0,0,1]
	v_and_b32_e32 v13, 0xffff0000, v91
	v_pk_mul_f32 v[64:65], v[6:7], v[30:31] op_sel_hi:[0,1]
	v_pk_mul_f32 v[30:31], v[38:39], v[62:63]
	v_lshlrev_b32_e32 v8, 16, v87
	v_pk_fma_f32 v[30:31], v[32:33], v[40:41], v[30:31]
	v_and_b32_e32 v9, 0xffff0000, v87
	v_pk_mul_f32 v[62:63], v[6:7], v[30:31] op_sel_hi:[0,1]
	v_mov_b32_e32 v31, v104
	v_mov_b32_e32 v28, v103
	v_mov_b32_e32 v30, v102
	v_mov_b32_e32 v29, v105
	v_pk_mul_f32 v[26:27], v[28:29], v[12:13]
	v_lshlrev_b32_e32 v40, 16, v92
	v_pk_fma_f32 v[26:27], v[30:31], v[8:9], v[26:27] neg_lo:[0,0,1] neg_hi:[0,0,1]
	v_pk_mul_f32 v[8:9], v[28:29], v[8:9]
	v_pk_mul_f32 v[66:67], v[6:7], v[26:27] op_sel_hi:[0,1]
	v_pk_fma_f32 v[8:9], v[30:31], v[12:13], v[8:9]
	v_and_b32_e32 v41, 0xffff0000, v92
	v_mov_b32_e32 v27, v100
	v_mov_b32_e32 v24, v99
	v_pk_mul_f32 v[12:13], v[6:7], v[8:9] op_sel_hi:[0,1]
	v_lshlrev_b32_e32 v8, 16, v88
	v_and_b32_e32 v9, 0xffff0000, v88
	v_mov_b32_e32 v26, v98
	v_mov_b32_e32 v25, v101
	v_pk_mul_f32 v[22:23], v[24:25], v[40:41]
	v_lshlrev_b32_e32 v10, 16, v93
	v_pk_fma_f32 v[22:23], v[26:27], v[8:9], v[22:23] neg_lo:[0,0,1] neg_hi:[0,0,1]
	v_pk_mul_f32 v[8:9], v[24:25], v[8:9]
	v_pk_mul_f32 v[22:23], v[6:7], v[22:23] op_sel_hi:[0,1]
	v_pk_fma_f32 v[8:9], v[26:27], v[40:41], v[8:9]
	v_mov_b32_e32 v41, v96
	v_pk_mul_f32 v[70:71], v[6:7], v[8:9] op_sel_hi:[0,1]
	v_lshlrev_b32_e32 v8, 16, v89
	v_and_b32_e32 v9, 0xffff0000, v89
	v_and_b32_e32 v11, 0xffff0000, v93
	v_mov_b32_e32 v20, v95
	v_mov_b32_e32 v40, v94
	v_mov_b32_e32 v21, v97
	v_pk_mul_f32 v[14:15], v[20:21], v[10:11]
	s_nop 0
	v_pk_fma_f32 v[14:15], v[40:41], v[8:9], v[14:15] neg_lo:[0,0,1] neg_hi:[0,0,1]
	v_pk_mul_f32 v[8:9], v[20:21], v[8:9]
	v_pk_mul_f32 v[14:15], v[6:7], v[14:15] op_sel_hi:[0,1]
	v_pk_fma_f32 v[8:9], v[40:41], v[10:11], v[8:9]
	s_nop 0
	v_pk_mul_f32 v[10:11], v[6:7], v[8:9] op_sel_hi:[0,1]
	v_cvt_pk_bf16_f32 v6, v64, v65
	v_cvt_pk_bf16_f32 v7, v66, v67
	v_cvt_pk_bf16_f32 v8, v22, v23
	v_cvt_pk_bf16_f32 v9, v14, v15
	v_add3_u32 v14, 0, v60, v58
	ds_write_b128 v14, v[6:9]
	v_cvt_pk_bf16_f32 v6, v62, v63
	v_cvt_pk_bf16_f32 v7, v12, v13
	v_cvt_pk_bf16_f32 v8, v70, v71
	v_cvt_pk_bf16_f32 v9, v10, v11
	v_add3_u32 v10, 0, v59, v58
	ds_write_b128 v10, v[6:9]
	v_mad_i64_i32 v[6:7], s[4:5], v34, s33, v[42:43]
	v_lshl_add_u64 v[6:7], v[6:7], 0, v[2:3]
	s_nop 0
	s_nop 0
	v_mul_f32_e32 v22, s0, v57
	v_exp_f32_e32 v22, v22
	v_readlane_b32 s4, v252, 30
	v_readlane_b32 s5, v252, 31
	v_mul_f32_e32 v42, 0x3db504f3, v22
	s_waitcnt vmcnt(17)
	v_lshlrev_b32_e32 v66, 16, v110
	s_waitcnt vmcnt(16)
	v_lshlrev_b32_e32 v74, 16, v114
	v_and_b32_e32 v75, 0xffff0000, v114
	s_waitcnt vmcnt(12)
; #define GAS __attribute__((address_space(1)))
; template <int MODE  > __device__ __forceinline__ void ret_stage_rot(LAS unsigned char* tile, const bf16* src  , const f32x2* rot  , float sc, float l2g, int tid) {
; #pragma unroll
;     for (int i = 0; i < 2; ++i) { const int item = tid + 512 * i, j = item >> 3, cc = item & 7;
;         const v4u lo = *(const GAS v4u*)(src + (size_t)j * LDP + 8 * cc), hh = *(const GAS v4u*)(src + (size_t)j * LDP + 64 + 8 * cc);
;         const GAS f32x4* rp = (const GAS f32x4*)(rot + (size_t)j * 64 + 8 * cc);
;         const f32x4 c0 = rp[0], c1 = rp[1], c2 = rp[2], c3 = rp[3];
;         const float cs[8] = {c0.x, c0.z, c1.x, c1.z, c2.x, c2.z, c3.x, c3.z}, sn[8] = {c0.y, c0.w, c1.y, c1.w, c2.y, c2.w, c3.y, c3.w};
;         const float a[8] = {bflo(lo.x), bfhi(lo.x), bflo(lo.y), bfhi(lo.y), bflo(lo.z), bfhi(lo.z), bflo(lo.w), bfhi(lo.w)};
;         const float bb[8] = {bflo(hh.x), bfhi(hh.x), bflo(hh.y), bfhi(hh.y), bflo(hh.z), bfhi(hh.z), bflo(hh.w), bfhi(hh.w)};
;         const float s = MODE == 1 ? sc * __builtin_amdgcn_exp2f((float)(127 - j) * l2g) : sc;
;         float o1[8], o2[8];
; #pragma unroll
;         for (int e = 0; e < 8; ++e) { o1[e] = (a[e] * cs[e] - bb[e] * sn[e]) * s; o2[e] = (bb[e] * cs[e] + a[e] * sn[e]) * s; }
;         v4u w; w.x = pk2(o1[0], o1[1]); w.y = pk2(o1[2], o1[3]); w.z = pk2(o1[4], o1[5]); w.w = pk2(o1[6], o1[7]); *(LAS v4u*)(tile + offb(j, cc)) = w;
;         w.x = pk2(o2[0], o2[1]); w.y = pk2(o2[2], o2[3]); w.z = pk2(o2[4], o2[5]); w.w = pk2(o2[6], o2[7]); *(LAS v4u*)(tile + offb(j, cc + 8)) = w; }
; }
; __device__ __forceinline__ void ret_stage_plain(LAS unsigned char* tile, const bf16* src, int ld, int tid) {
; #pragma unroll
;     for (int i = 0; i < 4; ++i) { const int item = tid + 512 * i, row = item >> 4, ch = item & 15; *(LAS v4u*)(tile + offb(row, ch)) = *(const GAS v4u*)(src + (size_t)row * ld + 8 * ch); }
; __device__ __forceinline__ void retA_unit2(LAS unsigned char* lds, const bf16* proj, const f32x2* rot, float* KV, int uA, int uB, int tid, int lane, int wid) {
;     ...
;     for (int s = 0; s < 2; ++s) { const int u = s ? uB : uA; const int bh = u >> 5, c = u & 31, b = bh >> 3, h = bh & 7; const size_t t0 = (size_t)b * SEQ + c * 128;
;         ret_stage_rot<1>(lds + s * 65536, proj + t0 * LDP + C_KR + h * 128, rot + (size_t)c * 128 * 64, RET_KSCALE, kLog2Gamma[h], tid);
	v_mov_b32_e32 v23, v132
	v_mov_b32_e32 v18, v131
	v_and_b32_e32 v67, 0xffff0000, v110
	v_mov_b32_e32 v22, v130
	v_mov_b32_e32 v19, v133
	v_pk_mul_f32 v[16:17], v[18:19], v[74:75]
	v_lshlrev_b32_e32 v70, 16, v115
	v_pk_fma_f32 v[16:17], v[22:23], v[66:67], v[16:17] neg_lo:[0,0,1] neg_hi:[0,0,1]
	v_and_b32_e32 v71, 0xffff0000, v115
	v_pk_mul_f32 v[76:77], v[42:43], v[16:17] op_sel_hi:[0,1]
	v_pk_mul_f32 v[16:17], v[22:23], v[74:75]
	v_lshlrev_b32_e32 v62, 16, v111
	v_pk_fma_f32 v[16:17], v[18:19], v[66:67], v[16:17]
	v_and_b32_e32 v63, 0xffff0000, v111
	v_pk_mul_f32 v[66:67], v[42:43], v[16:17] op_sel_hi:[0,1]
	v_mov_b32_e32 v17, v128
	v_mov_b32_e32 v14, v127
	v_mov_b32_e32 v16, v126
	v_mov_b32_e32 v15, v129
	v_pk_mul_f32 v[12:13], v[14:15], v[70:71]
	v_lshlrev_b32_e32 v78, 16, v116
	v_pk_fma_f32 v[12:13], v[16:17], v[62:63], v[12:13] neg_lo:[0,0,1] neg_hi:[0,0,1]
	v_and_b32_e32 v79, 0xffff0000, v116
	v_pk_mul_f32 v[74:75], v[42:43], v[12:13] op_sel_hi:[0,1]
	v_pk_mul_f32 v[12:13], v[14:15], v[62:63]
	v_lshlrev_b32_e32 v62, 16, v112
	v_pk_fma_f32 v[12:13], v[16:17], v[70:71], v[12:13]
	v_and_b32_e32 v63, 0xffff0000, v112
	v_pk_mul_f32 v[70:71], v[42:43], v[12:13] op_sel_hi:[0,1]
	v_mov_b32_e32 v13, v124
	v_mov_b32_e32 v10, v123
	v_mov_b32_e32 v12, v122
	v_mov_b32_e32 v11, v125
	v_pk_mul_f32 v[8:9], v[10:11], v[78:79]
	v_lshlrev_b32_e32 v64, 16, v117
	v_pk_fma_f32 v[8:9], v[12:13], v[62:63], v[8:9] neg_lo:[0,0,1] neg_hi:[0,0,1]
	s_nop 0
	v_pk_mul_f32 v[80:81], v[42:43], v[8:9] op_sel_hi:[0,1]
	v_pk_mul_f32 v[8:9], v[10:11], v[62:63]
	v_lshlrev_b32_e32 v62, 16, v113
	v_pk_fma_f32 v[8:9], v[12:13], v[78:79], v[8:9]
	v_and_b32_e32 v63, 0xffff0000, v113
	v_pk_mul_f32 v[78:79], v[42:43], v[8:9] op_sel_hi:[0,1]
	v_and_b32_e32 v65, 0xffff0000, v117
	v_mov_b32_e32 v9, v120
	v_mov_b32_e32 v6, v119
	v_mov_b32_e32 v8, v118
	v_mov_b32_e32 v7, v121
	v_pk_mul_f32 v[4:5], v[6:7], v[64:65]
	s_nop 0
	v_pk_fma_f32 v[4:5], v[8:9], v[62:63], v[4:5] neg_lo:[0,0,1] neg_hi:[0,0,1]
	v_pk_mul_f32 v[62:63], v[6:7], v[62:63]
	v_pk_mul_f32 v[4:5], v[42:43], v[4:5] op_sel_hi:[0,1]
	v_pk_fma_f32 v[62:63], v[8:9], v[64:65], v[62:63]
	v_cvt_pk_bf16_f32 v64, v80, v81
	v_pk_mul_f32 v[42:43], v[42:43], v[62:63] op_sel_hi:[0,1]
	v_cvt_pk_bf16_f32 v62, v76, v77
	v_cvt_pk_bf16_f32 v63, v74, v75
	v_cvt_pk_bf16_f32 v65, v4, v5
	v_add3_u32 v4, 0, v56, v54
	ds_write_b128 v4, v[62:65]
	v_cvt_pk_bf16_f32 v62, v66, v67
	v_cvt_pk_bf16_f32 v63, v70, v71
	v_cvt_pk_bf16_f32 v64, v78, v79
	v_cvt_pk_bf16_f32 v65, v42, v43
	v_add3_u32 v4, 0, v55, v54
	ds_write_b128 v4, v[62:65]
	v_lshlrev_b32_e32 v4, 4, v69
	v_mov_b32_e32 v5, v3
	v_lshl_add_u64 v[42:43], s[4:5], 0, v[4:5]
	v_mad_i64_i32 v[62:63], s[4:5], v52, s33, v[42:43]
	v_add3_u32 v66, 0, v53, v51
	s_waitcnt vmcnt(11)
	ds_write_b128 v66, v[134:137] offset:32768
	v_mad_i64_i32 v[62:63], s[4:5], v49, s33, v[42:43]
	v_add3_u32 v66, 0, v50, v47
	s_waitcnt vmcnt(10)
	ds_write_b128 v66, v[138:141] offset:32768
	v_mad_i64_i32 v[62:63], s[4:5], v46, s33, v[42:43]
	v_add3_u32 v66, 0, v48, v45
	v_mad_i64_i32 v[42:43], s[4:5], v44, s33, v[42:43]
	v_readlane_b32 s4, v252, 34
	v_readlane_b32 s5, v252, 35
	s_load_dword s5, s[4:5], 0x0
	s_add_i32 s4, 0, 0x10000
	s_waitcnt vmcnt(9)
	ds_write_b128 v66, v[142:145] offset:32768
	v_add3_u32 v42, 0, v37, v35
	s_waitcnt vmcnt(8)
	ds_write_b128 v42, v[146:149] offset:32768
	v_mov_b64_e32 v[42:43], s[18:19]
	v_mad_i64_i32 v[62:63], s[18:19], v36, s33, v[42:43]
	v_lshl_add_u64 v[66:67], v[62:63], 0, v[2:3]
	s_waitcnt lgkmcnt(0)
	v_mul_f32_e32 v36, s5, v61
	v_exp_f32_e32 v36, v36
	s_waitcnt vmcnt(7)
	v_lshlrev_b32_e32 v66, 16, v150
	s_waitcnt vmcnt(6)
	v_lshlrev_b32_e32 v74, 16, v154
	v_and_b32_e32 v75, 0xffff0000, v154
	v_and_b32_e32 v67, 0xffff0000, v150
	v_pk_mul_f32 v[76:77], v[32:33], v[74:75]
	v_lshlrev_b32_e32 v62, 16, v155
	v_pk_fma_f32 v[76:77], v[38:39], v[66:67], v[76:77] neg_lo:[0,0,1] neg_hi:[0,0,1]
	v_pk_mul_f32 v[38:39], v[38:39], v[74:75]
	v_mul_f32_e32 v36, 0x3db504f3, v36
	v_pk_fma_f32 v[32:33], v[32:33], v[66:67], v[38:39]
	v_lshlrev_b32_e32 v38, 16, v151
	v_and_b32_e32 v39, 0xffff0000, v151
	v_and_b32_e32 v63, 0xffff0000, v155
	v_pk_mul_f32 v[66:67], v[28:29], v[62:63]
	v_pk_mul_f32 v[76:77], v[36:37], v[76:77] op_sel_hi:[0,1]
	v_pk_fma_f32 v[66:67], v[30:31], v[38:39], v[66:67] neg_lo:[0,0,1] neg_hi:[0,0,1]
	v_pk_mul_f32 v[30:31], v[30:31], v[62:63]
	v_pk_mul_f32 v[66:67], v[36:37], v[66:67] op_sel_hi:[0,1]
	v_pk_fma_f32 v[28:29], v[28:29], v[38:39], v[30:31]
	v_lshlrev_b32_e32 v38, 16, v156
	v_and_b32_e32 v39, 0xffff0000, v156
	v_lshlrev_b32_e32 v30, 16, v152
	v_and_b32_e32 v31, 0xffff0000, v152
	v_pk_mul_f32 v[62:63], v[24:25], v[38:39]
	v_pk_mul_f32 v[32:33], v[36:37], v[32:33] op_sel_hi:[0,1]
	v_pk_fma_f32 v[62:63], v[26:27], v[30:31], v[62:63] neg_lo:[0,0,1] neg_hi:[0,0,1]
	v_pk_mul_f32 v[26:27], v[26:27], v[38:39]
	v_pk_mul_f32 v[62:63], v[36:37], v[62:63] op_sel_hi:[0,1]
	v_pk_fma_f32 v[24:25], v[24:25], v[30:31], v[26:27]
	v_lshlrev_b32_e32 v26, 16, v157
	v_and_b32_e32 v27, 0xffff0000, v157
	v_pk_mul_f32 v[30:31], v[36:37], v[24:25] op_sel_hi:[0,1]
	v_lshlrev_b32_e32 v24, 16, v153
	v_and_b32_e32 v25, 0xffff0000, v153
	v_pk_mul_f32 v[38:39], v[20:21], v[26:27]
	v_pk_mul_f32 v[26:27], v[40:41], v[26:27]
	v_pk_fma_f32 v[38:39], v[40:41], v[24:25], v[38:39] neg_lo:[0,0,1] neg_hi:[0,0,1]
	v_pk_fma_f32 v[20:21], v[20:21], v[24:25], v[26:27]
	v_pk_mul_f32 v[38:39], v[36:37], v[38:39] op_sel_hi:[0,1]
	v_pk_mul_f32 v[28:29], v[36:37], v[28:29] op_sel_hi:[0,1]
	v_pk_mul_f32 v[20:21], v[36:37], v[20:21] op_sel_hi:[0,1]
	v_cvt_pk_bf16_f32 v24, v76, v77
	v_cvt_pk_bf16_f32 v25, v66, v67
	v_cvt_pk_bf16_f32 v26, v62, v63
	v_cvt_pk_bf16_f32 v27, v38, v39
	v_add3_u32 v36, s4, v60, v58
	ds_write_b128 v36, v[24:27]
	v_cvt_pk_bf16_f32 v24, v32, v33
	v_cvt_pk_bf16_f32 v25, v28, v29
	v_cvt_pk_bf16_f32 v26, v30, v31
	v_cvt_pk_bf16_f32 v27, v20, v21
	v_add3_u32 v20, s4, v59, v58
	ds_write_b128 v20, v[24:27]
	v_mad_i64_i32 v[20:21], s[18:19], v34, s33, v[42:43]
	v_lshl_add_u64 v[20:21], v[20:21], 0, v[2:3]
	v_mul_f32_e32 v2, s5, v57
	v_exp_f32_e32 v2, v2
	v_readlane_b32 s18, v252, 36
	v_readlane_b32 s19, v252, 37
	s_add_i32 s5, 0, 0x18000
	v_mul_f32_e32 v2, 0x3db504f3, v2
	s_waitcnt vmcnt(5)
; #define GAS __attribute__((address_space(1)))
; template <int MODE  > __device__ __forceinline__ void ret_stage_rot(LAS unsigned char* tile, const bf16* src  , const f32x2* rot  , float sc, float l2g, int tid) {
; #pragma unroll
;     for (int i = 0; i < 2; ++i) { const int item = tid + 512 * i, j = item >> 3, cc = item & 7;
;         const v4u lo = *(const GAS v4u*)(src + (size_t)j * LDP + 8 * cc), hh = *(const GAS v4u*)(src + (size_t)j * LDP + 64 + 8 * cc);
;         const GAS f32x4* rp = (const GAS f32x4*)(rot + (size_t)j * 64 + 8 * cc);
;         const f32x4 c0 = rp[0], c1 = rp[1], c2 = rp[2], c3 = rp[3];
;         const float cs[8] = {c0.x, c0.z, c1.x, c1.z, c2.x, c2.z, c3.x, c3.z}, sn[8] = {c0.y, c0.w, c1.y, c1.w, c2.y, c2.w, c3.y, c3.w};
;         const float a[8] = {bflo(lo.x), bfhi(lo.x), bflo(lo.y), bfhi(lo.y), bflo(lo.z), bfhi(lo.z), bflo(lo.w), bfhi(lo.w)};
;         const float bb[8] = {bflo(hh.x), bfhi(hh.x), bflo(hh.y), bfhi(hh.y), bflo(hh.z), bfhi(hh.z), bflo(hh.w), bfhi(hh.w)};
;         const float s = MODE == 1 ? sc * __builtin_amdgcn_exp2f((float)(127 - j) * l2g) : sc;
;         float o1[8], o2[8];
; #pragma unroll
;         for (int e = 0; e < 8; ++e) { o1[e] = (a[e] * cs[e] - bb[e] * sn[e]) * s; o2[e] = (bb[e] * cs[e] + a[e] * sn[e]) * s; }
;         v4u w; w.x = pk2(o1[0], o1[1]); w.y = pk2(o1[2], o1[3]); w.z = pk2(o1[4], o1[5]); w.w = pk2(o1[6], o1[7]); *(LAS v4u*)(tile + offb(j, cc)) = w;
;         w.x = pk2(o2[0], o2[1]); w.y = pk2(o2[2], o2[3]); w.z = pk2(o2[4], o2[5]); w.w = pk2(o2[6], o2[7]); *(LAS v4u*)(tile + offb(j, cc + 8)) = w; }
; }
; __device__ __forceinline__ void ret_stage_plain(LAS unsigned char* tile, const bf16* src, int ld, int tid) {
; #pragma unroll
;     for (int i = 0; i < 4; ++i) { const int item = tid + 512 * i, row = item >> 4, ch = item & 15; *(LAS v4u*)(tile + offb(row, ch)) = *(const GAS v4u*)(src + (size_t)row * ld + 8 * ch); }
; __device__ __forceinline__ void retA_unit2(LAS unsigned char* lds, const bf16* proj, const f32x2* rot, float* KV, int uA, int uB, int tid, int lane, int wid) {
;     asm volatile("" : "+v"(tid)); lane = tid & 63;
;     const int hi = lane >> 5, r32 = lane & 31;
; #pragma unroll
;     for (int s = 0; s < 2; ++s) { const int u = s ? uB : uA; const int bh = u >> 5, c = u & 31, b = bh >> 3, h = bh & 7; const size_t t0 = (size_t)b * SEQ + c * 128;
	v_lshlrev_b32_e32 v20, 16, v158
	s_waitcnt vmcnt(4)
	v_lshlrev_b32_e32 v32, 16, v162
	v_and_b32_e32 v33, 0xffff0000, v162
	v_and_b32_e32 v21, 0xffff0000, v158
	v_pk_mul_f32 v[38:39], v[18:19], v[32:33]
	s_nop 0
	v_pk_fma_f32 v[38:39], v[22:23], v[20:21], v[38:39] neg_lo:[0,0,1] neg_hi:[0,0,1]
	v_pk_mul_f32 v[22:23], v[22:23], v[32:33]
	v_pk_mul_f32 v[38:39], v[2:3], v[38:39] op_sel_hi:[0,1]
	v_pk_fma_f32 v[18:19], v[18:19], v[20:21], v[22:23]
	v_lshlrev_b32_e32 v22, 16, v163
	v_and_b32_e32 v23, 0xffff0000, v163
	v_lshlrev_b32_e32 v20, 16, v159
	v_and_b32_e32 v21, 0xffff0000, v159
	v_pk_mul_f32 v[24:25], v[14:15], v[22:23]
	v_pk_mul_f32 v[18:19], v[2:3], v[18:19] op_sel_hi:[0,1]
	v_pk_fma_f32 v[24:25], v[16:17], v[20:21], v[24:25] neg_lo:[0,0,1] neg_hi:[0,0,1]
	v_pk_mul_f32 v[16:17], v[16:17], v[22:23]
	v_pk_mul_f32 v[24:25], v[2:3], v[24:25] op_sel_hi:[0,1]
	v_pk_fma_f32 v[14:15], v[14:15], v[20:21], v[16:17]
	v_lshlrev_b32_e32 v20, 16, v164
	v_and_b32_e32 v21, 0xffff0000, v164
	v_lshlrev_b32_e32 v16, 16, v160
	v_and_b32_e32 v17, 0xffff0000, v160
	v_pk_mul_f32 v[22:23], v[10:11], v[20:21]
	v_pk_mul_f32 v[14:15], v[2:3], v[14:15] op_sel_hi:[0,1]
	v_pk_fma_f32 v[22:23], v[12:13], v[16:17], v[22:23] neg_lo:[0,0,1] neg_hi:[0,0,1]
	v_pk_mul_f32 v[12:13], v[12:13], v[20:21]
	v_pk_mul_f32 v[22:23], v[2:3], v[22:23] op_sel_hi:[0,1]
	v_pk_fma_f32 v[10:11], v[10:11], v[16:17], v[12:13]
	v_lshlrev_b32_e32 v16, 16, v165
	v_and_b32_e32 v17, 0xffff0000, v165
	v_lshlrev_b32_e32 v12, 16, v161
	v_and_b32_e32 v13, 0xffff0000, v161
	v_pk_mul_f32 v[20:21], v[6:7], v[16:17]
	v_pk_mul_f32 v[10:11], v[2:3], v[10:11] op_sel_hi:[0,1]
	v_pk_fma_f32 v[20:21], v[8:9], v[12:13], v[20:21] neg_lo:[0,0,1] neg_hi:[0,0,1]
	v_pk_mul_f32 v[8:9], v[8:9], v[16:17]
	v_pk_mul_f32 v[20:21], v[2:3], v[20:21] op_sel_hi:[0,1]
	v_pk_fma_f32 v[6:7], v[6:7], v[12:13], v[8:9]
	v_cvt_pk_bf16_f32 v8, v22, v23
	v_pk_mul_f32 v[12:13], v[2:3], v[6:7] op_sel_hi:[0,1]
	v_cvt_pk_bf16_f32 v6, v38, v39
	v_cvt_pk_bf16_f32 v7, v24, v25
	v_cvt_pk_bf16_f32 v9, v20, v21
	v_add3_u32 v2, s4, v56, v54
	ds_write_b128 v2, v[6:9]
	v_cvt_pk_bf16_f32 v6, v18, v19
	v_cvt_pk_bf16_f32 v7, v14, v15
	v_cvt_pk_bf16_f32 v8, v10, v11
	v_cvt_pk_bf16_f32 v9, v12, v13
	v_add3_u32 v2, s4, v55, v54
	ds_write_b128 v2, v[6:9]
	v_lshl_add_u64 v[8:9], s[18:19], 0, v[4:5]
	v_mad_i64_i32 v[4:5], s[18:19], v52, s33, v[8:9]
	v_add3_u32 v2, s5, v53, v51
	v_lshlrev_b32_e32 v11, 3, v68
	v_and_b32_e32 v11, 8, v11
	s_waitcnt vmcnt(3)
	ds_write_b128 v2, v[166:169]
	v_mad_i64_i32 v[4:5], s[18:19], v49, s33, v[8:9]
	v_add3_u32 v2, s5, v50, v47
	s_waitcnt vmcnt(2)
	ds_write_b128 v2, v[170:173]
	v_mad_i64_i32 v[4:5], s[18:19], v46, s33, v[8:9]
	v_add3_u32 v2, s5, v48, v45
	s_waitcnt vmcnt(1)
	ds_write_b128 v2, v[174:177]
	v_mad_i64_i32 v[4:5], s[18:19], v44, s33, v[8:9]
	v_add3_u32 v2, s5, v37, v35
	v_readlane_b32 s18, v252, 38
	v_readlane_b32 s19, v252, 39
	s_waitcnt vmcnt(0)
	ds_write_b128 v2, v[178:181]
	v_lshrrev_b32_e32 v2, 2, v68
	v_lshrrev_b32_e32 v4, 3, v68
	v_and_b32_e32 v2, 11, v2
	v_and_b32_e32 v4, 2, v4
	v_lshrrev_b32_e32 v5, 1, v68
	v_and_or_b32 v4, v5, 1, v4
	v_lshlrev_b32_e32 v6, 8, v2
	v_lshrrev_b32_e32 v8, 2, v2
	v_or_b32_e32 v2, 4, v2
	v_or_b32_e32 v5, s95, v4
	v_and_b32_e32 v7, 12, v68
	v_lshlrev_b32_e32 v12, 8, v2
	v_lshrrev_b32_e32 v2, 2, v2
	v_or_b32_e32 v9, v8, v7
	v_bitop3_b32 v10, v8, v5, v7 bitop3:0x36
	v_or_b32_e32 v13, v11, v6
	v_or_b32_e32 v14, v11, v12
	v_bitop3_b32 v8, v8, v4, v7 bitop3:0x36
	v_bitop3_b32 v15, v2, v4, v7 bitop3:0x36
	v_bitop3_b32 v5, v2, v5, v7 bitop3:0x36
	v_or_b32_e32 v16, 4, v4
	v_bitop3_b32 v17, v4, v9, 4 bitop3:0x36
	v_or_b32_e32 v18, 8, v4
	v_bitop3_b32 v19, v4, v9, 8 bitop3:0x36
	v_or_b32_e32 v20, 12, v4
	v_bitop3_b32 v69, v4, v9, 12 bitop3:0x36
	v_lshl_add_u32 v4, v10, 4, s51
	v_lshl_or_b32 v8, v8, 4, v13
	v_lshl_or_b32 v10, v15, 4, v14
	s_waitcnt vmcnt(0) lgkmcnt(0)
	v_mov_b32_e32 v26, v160
	v_mov_b32_e32 v27, v161
	v_mov_b32_e32 v28, v162
	v_mov_b32_e32 v29, v163
	v_mov_b32_e32 v30, v164
	v_mov_b32_e32 v31, v165
	v_mov_b32_e32 v64, v152
	v_mov_b32_e32 v65, v153
	v_mov_b32_e32 v70, v154
	v_mov_b32_e32 v71, v155
	v_mov_b32_e32 v72, v156
	v_mov_b32_e32 v73, v157
	s_barrier
	v_mov_b32_e32 v202, v1
	v_ashrrev_i32_e32 v203, 3, v202
	v_and_b32_e32 v204, 7, v202
	v_readlane_b32 s100, v252, 40
	v_readlane_b32 s101, v252, 41
	s_nop 1
	v_mov_b64_e32 v[206:207], s[100:101]
	v_mad_i64_i32 v[208:209], s[100:101], v203, s33, v[206:207]
	v_lshlrev_b32_e32 v210, 4, v204
	v_mov_b32_e32 v212, v210
	v_mov_b32_e32 v213, v3
	v_lshl_add_u64 v[214:215], v[208:209], 0, v[212:213]
	global_load_dwordx4 v[86:89], v[214:215], off
	v_mov_b32_e32 v202, v1
	v_ashrrev_i32_e32 v203, 3, v202
	v_and_b32_e32 v204, 7, v202
	v_readlane_b32 s100, v252, 40
	v_readlane_b32 s101, v252, 41
	s_nop 1
	v_mov_b64_e32 v[206:207], s[100:101]
	v_mad_i64_i32 v[208:209], s[100:101], v203, s33, v[206:207]
	v_lshlrev_b32_e32 v210, 4, v204
	v_mov_b32_e32 v212, v210
	v_mov_b32_e32 v213, v3
	v_lshl_add_u64 v[214:215], v[208:209], 0, v[212:213]
	global_load_dwordx4 v[90:93], v[214:215], off offset:128
	v_mov_b32_e32 v202, v1
	v_ashrrev_i32_e32 v203, 3, v202
	v_and_b32_e32 v204, 7, v202
	v_ashrrev_i32_e32 v205, 31, v203
	v_mov_b32_e32 v206, v203
	v_mov_b32_e32 v207, v205
	v_lshlrev_b64 v[208:209], 9, v[206:207]
	v_lshlrev_b32_e32 v210, 6, v204
	v_mov_b32_e32 v212, v210
	v_mov_b32_e32 v213, v3
	v_lshl_add_u64 v[214:215], s[24:25], 0, v[212:213]
	v_lshl_add_u64 v[216:217], v[214:215], 0, v[208:209]
	global_load_dwordx4 v[94:97], v[216:217], off offset:48
	v_mov_b32_e32 v202, v1
	v_ashrrev_i32_e32 v203, 3, v202
	v_and_b32_e32 v204, 7, v202
; #define GAS __attribute__((address_space(1)))
; template <int MODE  > __device__ __forceinline__ void ret_stage_rot(LAS unsigned char* tile, const bf16* src  , const f32x2* rot  , float sc, float l2g, int tid) {
; #pragma unroll
;     for (int i = 0; i < 2; ++i) { const int item = tid + 512 * i, j = item >> 3, cc = item & 7;
;         const v4u lo = *(const GAS v4u*)(src + (size_t)j * LDP + 8 * cc), hh = *(const GAS v4u*)(src + (size_t)j * LDP + 64 + 8 * cc);
;         const GAS f32x4* rp = (const GAS f32x4*)(rot + (size_t)j * 64 + 8 * cc);
;         const f32x4 c0 = rp[0], c1 = rp[1], c2 = rp[2], c3 = rp[3];
;         const float cs[8] = {c0.x, c0.z, c1.x, c1.z, c2.x, c2.z, c3.x, c3.z}, sn[8] = {c0.y, c0.w, c1.y, c1.w, c2.y, c2.w, c3.y, c3.w};
;         const float a[8] = {bflo(lo.x), bfhi(lo.x), bflo(lo.y), bfhi(lo.y), bflo(lo.z), bfhi(lo.z), bflo(lo.w), bfhi(lo.w)};
;         const float bb[8] = {bflo(hh.x), bfhi(hh.x), bflo(hh.y), bfhi(hh.y), bflo(hh.z), bfhi(hh.z), bflo(hh.w), bfhi(hh.w)};
;         const float s = MODE == 1 ? sc * __builtin_amdgcn_exp2f((float)(127 - j) * l2g) : sc;
;         float o1[8], o2[8];
; #pragma unroll
;         for (int e = 0; e < 8; ++e) { o1[e] = (a[e] * cs[e] - bb[e] * sn[e]) * s; o2[e] = (bb[e] * cs[e] + a[e] * sn[e]) * s; }
;         v4u w; w.x = pk2(o1[0], o1[1]); w.y = pk2(o1[2], o1[3]); w.z = pk2(o1[4], o1[5]); w.w = pk2(o1[6], o1[7]); *(LAS v4u*)(tile + offb(j, cc)) = w;
;         w.x = pk2(o2[0], o2[1]); w.y = pk2(o2[2], o2[3]); w.z = pk2(o2[4], o2[5]); w.w = pk2(o2[6], o2[7]); *(LAS v4u*)(tile + offb(j, cc + 8)) = w; }
; }
; __device__ __forceinline__ void ret_stage_plain(LAS unsigned char* tile, const bf16* src, int ld, int tid) {
; #pragma unroll
;     for (int i = 0; i < 4; ++i) { const int item = tid + 512 * i, row = item >> 4, ch = item & 15; *(LAS v4u*)(tile + offb(row, ch)) = *(const GAS v4u*)(src + (size_t)row * ld + 8 * ch); }
; __device__ __forceinline__ void retA_unit2(LAS unsigned char* lds, const bf16* proj, const f32x2* rot, float* KV, int uA, int uB, int tid, int lane, int wid) {
;     ...
;     for (int s = 0; s < 2; ++s) { const int u = s ? uB : uA; const int bh = u >> 5, c = u & 31, b = bh >> 3, h = bh & 7; const size_t t0 = (size_t)b * SEQ + c * 128;
;         ret_stage_rot<1>(lds + s * 65536, proj + t0 * LDP + C_KR + h * 128, rot + (size_t)c * 128 * 64, RET_KSCALE, kLog2Gamma[h], tid);
	v_ashrrev_i32_e32 v205, 31, v203
	v_mov_b32_e32 v206, v203
	v_mov_b32_e32 v207, v205
	v_lshlrev_b64 v[208:209], 9, v[206:207]
	v_lshlrev_b32_e32 v210, 6, v204
	v_mov_b32_e32 v212, v210
	v_mov_b32_e32 v213, v3
	v_lshl_add_u64 v[214:215], s[24:25], 0, v[212:213]
	v_lshl_add_u64 v[216:217], v[214:215], 0, v[208:209]
	global_load_dwordx4 v[98:101], v[216:217], off offset:32
	v_mov_b32_e32 v202, v1
	v_ashrrev_i32_e32 v203, 3, v202
	v_and_b32_e32 v204, 7, v202
	v_ashrrev_i32_e32 v205, 31, v203
	v_mov_b32_e32 v206, v203
	v_mov_b32_e32 v207, v205
	v_lshlrev_b64 v[208:209], 9, v[206:207]
	v_lshlrev_b32_e32 v210, 6, v204
	v_mov_b32_e32 v212, v210
	v_mov_b32_e32 v213, v3
	v_lshl_add_u64 v[214:215], s[24:25], 0, v[212:213]
	v_lshl_add_u64 v[216:217], v[214:215], 0, v[208:209]
	global_load_dwordx4 v[102:105], v[216:217], off offset:16
	v_mov_b32_e32 v202, v1
	v_ashrrev_i32_e32 v203, 3, v202
	v_and_b32_e32 v204, 7, v202
	v_ashrrev_i32_e32 v205, 31, v203
	v_mov_b32_e32 v206, v203
	v_mov_b32_e32 v207, v205
	v_lshlrev_b64 v[208:209], 9, v[206:207]
	v_lshlrev_b32_e32 v210, 6, v204
	v_mov_b32_e32 v212, v210
	v_mov_b32_e32 v213, v3
	v_lshl_add_u64 v[214:215], s[24:25], 0, v[212:213]
	v_lshl_add_u64 v[216:217], v[214:215], 0, v[208:209]
	global_load_dwordx4 v[106:109], v[216:217], off
	v_mov_b32_e32 v202, v1
	v_and_b32_e32 v203, 7, v202
	v_add_u32_e32 v204, 0x200, v202
	v_ashrrev_i32_e32 v205, 3, v204
	v_readlane_b32 s100, v252, 40
	v_readlane_b32 s101, v252, 41
	s_nop 1
	v_mov_b64_e32 v[206:207], s[100:101]
	v_lshlrev_b32_e32 v208, 4, v203
	v_mad_i64_i32 v[210:211], s[100:101], v205, s33, v[206:207]
	v_mov_b32_e32 v212, v208
	v_mov_b32_e32 v213, v3
	v_lshl_add_u64 v[214:215], v[210:211], 0, v[212:213]
	global_load_dwordx4 v[110:113], v[214:215], off
	v_mov_b32_e32 v202, v1
	v_and_b32_e32 v203, 7, v202
	v_add_u32_e32 v204, 0x200, v202
	v_ashrrev_i32_e32 v205, 3, v204
	v_readlane_b32 s100, v252, 40
	v_readlane_b32 s101, v252, 41
	s_nop 1
	v_mov_b64_e32 v[206:207], s[100:101]
	v_lshlrev_b32_e32 v208, 4, v203
	v_mad_i64_i32 v[210:211], s[100:101], v205, s33, v[206:207]
	v_mov_b32_e32 v212, v208
	v_mov_b32_e32 v213, v3
	v_lshl_add_u64 v[214:215], v[210:211], 0, v[212:213]
	global_load_dwordx4 v[114:117], v[214:215], off offset:128
	v_mov_b32_e32 v202, v1
	v_and_b32_e32 v203, 7, v202
	v_add_u32_e32 v204, 0x200, v202
	v_ashrrev_i32_e32 v205, 3, v204
	v_lshlrev_b32_e32 v206, 6, v203
	v_mov_b32_e32 v208, v206
	v_mov_b32_e32 v209, v3
	v_lshl_add_u64 v[210:211], s[24:25], 0, v[208:209]
	v_ashrrev_i32_e32 v212, 31, v205
	v_mov_b32_e32 v214, v205
	v_mov_b32_e32 v215, v212
	v_lshlrev_b64 v[216:217], 9, v[214:215]
	v_lshl_add_u64 v[218:219], v[210:211], 0, v[216:217]
	global_load_dwordx4 v[118:121], v[218:219], off offset:48
	v_mov_b32_e32 v202, v1
	v_and_b32_e32 v203, 7, v202
	v_add_u32_e32 v204, 0x200, v202
	v_ashrrev_i32_e32 v205, 3, v204
	v_lshlrev_b32_e32 v206, 6, v203
	v_mov_b32_e32 v208, v206
	v_mov_b32_e32 v209, v3
	v_lshl_add_u64 v[210:211], s[24:25], 0, v[208:209]
	v_ashrrev_i32_e32 v212, 31, v205
	v_mov_b32_e32 v214, v205
	v_mov_b32_e32 v215, v212
	v_lshlrev_b64 v[216:217], 9, v[214:215]
	v_lshl_add_u64 v[218:219], v[210:211], 0, v[216:217]
	global_load_dwordx4 v[122:125], v[218:219], off offset:32
	v_mov_b32_e32 v202, v1
	v_and_b32_e32 v203, 7, v202
	v_add_u32_e32 v204, 0x200, v202
	v_ashrrev_i32_e32 v205, 3, v204
	v_lshlrev_b32_e32 v206, 6, v203
	v_mov_b32_e32 v208, v206
	v_mov_b32_e32 v209, v3
	v_lshl_add_u64 v[210:211], s[24:25], 0, v[208:209]
	v_ashrrev_i32_e32 v212, 31, v205
	v_mov_b32_e32 v214, v205
	v_mov_b32_e32 v215, v212
	v_lshlrev_b64 v[216:217], 9, v[214:215]
	v_lshl_add_u64 v[218:219], v[210:211], 0, v[216:217]
	global_load_dwordx4 v[126:129], v[218:219], off offset:16
	v_mov_b32_e32 v202, v1
	v_and_b32_e32 v203, 7, v202
	v_add_u32_e32 v204, 0x200, v202
	v_ashrrev_i32_e32 v205, 3, v204
	v_lshlrev_b32_e32 v206, 6, v203
	v_mov_b32_e32 v208, v206
	v_mov_b32_e32 v209, v3
	v_lshl_add_u64 v[210:211], s[24:25], 0, v[208:209]
	v_ashrrev_i32_e32 v212, 31, v205
	v_mov_b32_e32 v214, v205
	v_mov_b32_e32 v215, v212
	v_lshlrev_b64 v[216:217], 9, v[214:215]
	v_lshl_add_u64 v[218:219], v[210:211], 0, v[216:217]
	global_load_dwordx4 v[130:133], v[218:219], off
	v_mov_b32_e32 v202, v1
	v_ashrrev_i32_e32 v203, 4, v202
	v_and_b32_e32 v204, 15, v202
	v_readlane_b32 s100, v252, 44
	v_readlane_b32 s101, v252, 45
	v_lshlrev_b32_e32 v205, 4, v204
	v_mov_b32_e32 v206, v3
	v_mov_b32_e32 v208, v205
	v_mov_b32_e32 v209, v206
	v_lshl_add_u64 v[210:211], s[100:101], 0, v[208:209]
	v_mad_i64_i32 v[212:213], s[100:101], v203, s33, v[210:211]
	global_load_dwordx4 v[134:137], v[212:213], off
	v_mov_b32_e32 v202, v1
	v_add_u32_e32 v203, 0x200, v202
	v_and_b32_e32 v204, 15, v202
	v_ashrrev_i32_e32 v205, 4, v203
	v_readlane_b32 s100, v252, 44
	v_readlane_b32 s101, v252, 45
	v_lshlrev_b32_e32 v206, 4, v204
	v_mov_b32_e32 v207, v3
	v_lshl_add_u64 v[208:209], s[100:101], 0, v[206:207]
	v_mad_i64_i32 v[210:211], s[100:101], v205, s33, v[208:209]
	global_load_dwordx4 v[138:141], v[210:211], off
	v_mov_b32_e32 v202, v1
	v_and_b32_e32 v203, 15, v202
	v_add_u32_e32 v204, 0x400, v202
	v_ashrrev_i32_e32 v205, 4, v204
	v_readlane_b32 s100, v252, 44
	v_readlane_b32 s101, v252, 45
	v_lshlrev_b32_e32 v206, 4, v203
	v_mov_b32_e32 v207, v3
	v_lshl_add_u64 v[208:209], s[100:101], 0, v[206:207]
	v_mad_i64_i32 v[210:211], s[100:101], v205, s33, v[208:209]
	global_load_dwordx4 v[142:145], v[210:211], off
	v_mov_b32_e32 v202, v1
	v_and_b32_e32 v203, 15, v202
	v_add_u32_e32 v204, 0x600, v202
	v_ashrrev_i32_e32 v205, 4, v204
	v_readlane_b32 s100, v252, 44
	v_readlane_b32 s101, v252, 45
	v_lshlrev_b32_e32 v206, 4, v203
; #define LAS __attribute__((address_space(3)))
; __device__ __forceinline__ unsigned tr_off(int lane, int c, int t) { const int h = lane >> 5, blk = (lane >> 4) & 1, q = (lane & 15) >> 2, p = lane & 3; return offb(8 * h + 4 * t + q, 4 * c + 2 * blk + (p >> 1)) + 8u * (unsigned)(p & 1); }
; __device__ __forceinline__ bf16x8 trfrag(LAS unsigned char* tile, unsigned o0, unsigned o1) { const s16x4 a = ldtr(tile + o0), b = ldtr(tile + o1); return (bf16x8){a[0], a[1], a[2], a[3], b[0], b[1], b[2], b[3]}; }
; #define MFMA32(a, b, c) __builtin_amdgcn_mfma_f32_32x32x16_bf16((a), (b), (c), 0, 0, 0)
; __device__ __forceinline__ void retA_unit2(LAS unsigned char* lds, const bf16* proj, const f32x2* rot, float* KV, int uA, int uB, int tid, int lane, int wid) {
;     ...
;     for (int s = 0; s < 2; ++s) { const int u = s ? uB : uA; const int bh = u >> 5, c = u & 31, b = bh >> 3, h = bh & 7; const size_t t0 = (size_t)b * SEQ + c * 128;
;         ret_stage_rot<1>(lds + s * 65536, proj + t0 * LDP + C_KR + h * 128, rot + (size_t)c * 128 * 64, RET_KSCALE, kLog2Gamma[h], tid);
;         ret_stage_plain(lds + s * 65536 + 32768, proj + t0 * LDP + C_VR + h * 128, LDP, tid); }
;     ...
;     const int half = wid >> 2, db = wid & 3, u = half ? uB : uA;
;     LAS unsigned char* base = lds + half * 65536;
;     const unsigned a0 = tr_off(lane, db, 0), a1 = tr_off(lane, db, 1);
;     unsigned b0[4], b1[4];
; #pragma unroll
;     for (int k = 0; k < 4; ++k) { b0[k] = 32768u + tr_off(lane, k, 0); b1[k] = 32768u + tr_off(lane, k, 1); }
;     f32x16 acc[4] = {splat16(0.f), splat16(0.f), splat16(0.f), splat16(0.f)};
; #pragma unroll
;     for (int ks = 0; ks < 8; ++ks) { const bf16x8 A = trfrag(base, a0 + 4096u * ks, a1 + 4096u * ks);
; #pragma unroll
;         for (int k = 0; k < 4; ++k) { const bf16x8 B = trfrag(base, b0[k] + 4096u * ks, b1[k] + 4096u * ks); acc[k] = MFMA32(A, B, acc[k]); } }
	v_mov_b32_e32 v207, v3
	v_lshl_add_u64 v[208:209], s[100:101], 0, v[206:207]
	v_mad_i64_i32 v[210:211], s[100:101], v205, s33, v[208:209]
	global_load_dwordx4 v[146:149], v[210:211], off
	v_mov_b32_e32 v202, v1
	v_ashrrev_i32_e32 v203, 3, v202
	v_and_b32_e32 v204, 7, v202
	v_lshlrev_b32_e32 v205, 4, v204
	v_readlane_b32 s100, v252, 48
	v_readlane_b32 s101, v252, 49
	s_nop 1
	v_mov_b64_e32 v[206:207], s[100:101]
	v_mad_i64_i32 v[208:209], s[100:101], v203, s33, v[206:207]
	v_mov_b32_e32 v210, v205
	v_mov_b32_e32 v211, v3
	v_lshl_add_u64 v[212:213], v[208:209], 0, v[210:211]
	global_load_dwordx4 v[150:153], v[212:213], off
	v_mov_b32_e32 v202, v1
	v_ashrrev_i32_e32 v203, 3, v202
	v_and_b32_e32 v204, 7, v202
	v_lshlrev_b32_e32 v205, 4, v204
	v_readlane_b32 s100, v252, 48
	v_readlane_b32 s101, v252, 49
	s_nop 1
	v_mov_b64_e32 v[206:207], s[100:101]
	v_mad_i64_i32 v[208:209], s[100:101], v203, s33, v[206:207]
	v_mov_b32_e32 v210, v205
	v_mov_b32_e32 v211, v3
	v_lshl_add_u64 v[212:213], v[208:209], 0, v[210:211]
	global_load_dwordx4 v[154:157], v[212:213], off offset:128
	v_mov_b32_e32 v202, v1
	v_and_b32_e32 v203, 7, v202
	v_add_u32_e32 v204, 0x200, v202
	v_ashrrev_i32_e32 v205, 3, v204
	v_lshlrev_b32_e32 v206, 4, v203
	v_readlane_b32 s100, v252, 48
	v_readlane_b32 s101, v252, 49
	s_nop 1
	v_mov_b64_e32 v[208:209], s[100:101]
	v_mad_i64_i32 v[210:211], s[100:101], v205, s33, v[208:209]
	v_mov_b32_e32 v212, v206
	v_mov_b32_e32 v213, v3
	v_lshl_add_u64 v[214:215], v[210:211], 0, v[212:213]
	global_load_dwordx4 v[158:161], v[214:215], off
	v_mov_b32_e32 v202, v1
	v_and_b32_e32 v203, 7, v202
	v_add_u32_e32 v204, 0x200, v202
	v_ashrrev_i32_e32 v205, 3, v204
	v_lshlrev_b32_e32 v206, 4, v203
	v_readlane_b32 s100, v252, 48
	v_readlane_b32 s101, v252, 49
	s_nop 1
	v_mov_b64_e32 v[208:209], s[100:101]
	v_mad_i64_i32 v[210:211], s[100:101], v205, s33, v[208:209]
	v_mov_b32_e32 v212, v206
	v_mov_b32_e32 v213, v3
	v_lshl_add_u64 v[214:215], v[210:211], 0, v[212:213]
	global_load_dwordx4 v[162:165], v[214:215], off offset:128
	v_mov_b32_e32 v202, v1
	v_ashrrev_i32_e32 v203, 4, v202
	v_and_b32_e32 v204, 15, v202
	v_lshlrev_b32_e32 v205, 4, v204
	v_mov_b32_e32 v206, v3
	v_readlane_b32 s100, v252, 54
	v_readlane_b32 s101, v252, 55
	v_mov_b32_e32 v208, v205
	v_mov_b32_e32 v209, v206
	v_lshl_add_u64 v[210:211], s[100:101], 0, v[208:209]
	v_mad_i64_i32 v[212:213], s[100:101], v203, s33, v[210:211]
	global_load_dwordx4 v[166:169], v[212:213], off
	v_mov_b32_e32 v202, v1
	v_add_u32_e32 v203, 0x200, v202
	v_and_b32_e32 v204, 15, v202
	v_ashrrev_i32_e32 v205, 4, v203
	v_lshlrev_b32_e32 v206, 4, v204
	v_mov_b32_e32 v207, v3
	v_readlane_b32 s100, v252, 54
	v_readlane_b32 s101, v252, 55
	s_nop 1
	v_lshl_add_u64 v[208:209], s[100:101], 0, v[206:207]
	v_mad_i64_i32 v[210:211], s[100:101], v205, s33, v[208:209]
	global_load_dwordx4 v[170:173], v[210:211], off
	v_mov_b32_e32 v202, v1
	v_and_b32_e32 v203, 15, v202
	v_add_u32_e32 v204, 0x400, v202
	v_ashrrev_i32_e32 v205, 4, v204
	v_lshlrev_b32_e32 v206, 4, v203
	v_mov_b32_e32 v207, v3
	v_readlane_b32 s100, v252, 54
	v_readlane_b32 s101, v252, 55
	s_nop 1
	v_lshl_add_u64 v[208:209], s[100:101], 0, v[206:207]
	v_mad_i64_i32 v[210:211], s[100:101], v205, s33, v[208:209]
	global_load_dwordx4 v[174:177], v[210:211], off
	v_mov_b32_e32 v202, v1
	v_and_b32_e32 v203, 15, v202
	v_add_u32_e32 v204, 0x600, v202
	v_ashrrev_i32_e32 v205, 4, v204
	v_lshlrev_b32_e32 v206, 4, v203
	v_mov_b32_e32 v207, v3
	v_readlane_b32 s100, v252, 54
	v_readlane_b32 s101, v252, 55
	s_nop 1
	v_lshl_add_u64 v[208:209], s[100:101], 0, v[206:207]
	v_mad_i64_i32 v[210:211], s[100:101], v205, s33, v[208:209]
	global_load_dwordx4 v[178:181], v[210:211], off
	v_add3_u32 v77, v4, v6, v11
	v_lshl_add_u32 v4, v5, 4, s51
	v_add_u32_e32 v76, s51, v8
	v_add_u32_e32 v74, s51, v10
	v_bitop3_b32 v16, v2, v16, v7 bitop3:0x36
	v_bitop3_b32 v18, v2, v18, v7 bitop3:0x36
	v_bitop3_b32 v2, v2, v20, v7 bitop3:0x36
	v_add3_u32 v75, v4, v12, v11
	ds_read_b64_tr_b16 v[4:5], v77
	ds_read_b64_tr_b16 v[6:7], v75
	ds_read_b64_tr_b16 v[8:9], v76 offset:32768
	ds_read_b64_tr_b16 v[10:11], v74 offset:32768
	s_waitcnt lgkmcnt(0)
	v_mfma_f32_32x32x16_bf16 v[52:67], v[4:7], v[8:11], 0
	v_lshl_or_b32 v8, v17, 4, v13
	v_lshl_or_b32 v10, v16, 4, v14
	v_add_u32_e32 v73, s51, v8
	v_add_u32_e32 v72, s51, v10
	ds_read_b64_tr_b16 v[8:9], v73 offset:32768
	ds_read_b64_tr_b16 v[10:11], v72 offset:32768
	v_lshl_or_b32 v2, v2, 4, v14
	s_waitcnt lgkmcnt(0)
	v_mfma_f32_32x32x16_bf16 v[36:51], v[4:7], v[8:11], 0
	v_lshl_or_b32 v8, v19, 4, v13
	v_lshl_or_b32 v10, v18, 4, v14
	v_add_u32_e32 v71, s51, v8
	v_add_u32_e32 v70, s51, v10
	ds_read_b64_tr_b16 v[8:9], v71 offset:32768
	ds_read_b64_tr_b16 v[10:11], v70 offset:32768
	v_add_u32_e32 v2, s51, v2
	s_waitcnt lgkmcnt(0)
	v_mfma_f32_32x32x16_bf16 v[20:35], v[4:7], v[8:11], 0
	v_lshl_or_b32 v8, v69, 4, v13
	v_add_u32_e32 v69, s51, v8
	ds_read_b64_tr_b16 v[8:9], v69 offset:32768
	ds_read_b64_tr_b16 v[10:11], v2 offset:32768
	ds_read_b64_tr_b16 v[78:79], v77 offset:4096
	ds_read_b64_tr_b16 v[80:81], v75 offset:4096
	ds_read_b64_tr_b16 v[82:83], v76 offset:36864
	ds_read_b64_tr_b16 v[84:85], v74 offset:36864
	s_waitcnt lgkmcnt(0)
	v_mfma_f32_32x32x16_bf16 v[52:67], v[78:81], v[82:85], v[52:67]
	ds_read_b64_tr_b16 v[82:83], v73 offset:36864
	ds_read_b64_tr_b16 v[84:85], v72 offset:36864
	s_waitcnt lgkmcnt(0)
	v_mfma_f32_32x32x16_bf16 v[36:51], v[78:81], v[82:85], v[36:51]
	ds_read_b64_tr_b16 v[82:83], v71 offset:36864
	ds_read_b64_tr_b16 v[84:85], v70 offset:36864
	v_mfma_f32_32x32x16_bf16 v[4:19], v[4:7], v[8:11], 0
	s_waitcnt lgkmcnt(0)
; __device__ __forceinline__ bf16x8 trfrag(LAS unsigned char* tile, unsigned o0, unsigned o1) { const s16x4 a = ldtr(tile + o0), b = ldtr(tile + o1); return (bf16x8){a[0], a[1], a[2], a[3], b[0], b[1], b[2], b[3]}; }
; #define MFMA32(a, b, c) __builtin_amdgcn_mfma_f32_32x32x16_bf16((a), (b), (c), 0, 0, 0)
; __device__ __forceinline__ void retA_unit2(LAS unsigned char* lds, const bf16* proj, const f32x2* rot, float* KV, int uA, int uB, int tid, int lane, int wid) {
;     ...
; #pragma unroll
;     for (int ks = 0; ks < 8; ++ks) { const bf16x8 A = trfrag(base, a0 + 4096u * ks, a1 + 4096u * ks);
; #pragma unroll
;         for (int k = 0; k < 4; ++k) { const bf16x8 B = trfrag(base, b0[k] + 4096u * ks, b1[k] + 4096u * ks); acc[k] = MFMA32(A, B, acc[k]); } }
	v_mfma_f32_32x32x16_bf16 v[20:35], v[78:81], v[82:85], v[20:35]
	ds_read_b64_tr_b16 v[82:83], v69 offset:36864
	ds_read_b64_tr_b16 v[84:85], v2 offset:36864
	s_waitcnt lgkmcnt(0)
	v_mfma_f32_32x32x16_bf16 v[4:19], v[78:81], v[82:85], v[4:19]
	ds_read_b64_tr_b16 v[78:79], v77 offset:8192
	ds_read_b64_tr_b16 v[80:81], v75 offset:8192
	ds_read_b64_tr_b16 v[82:83], v76 offset:40960
	ds_read_b64_tr_b16 v[84:85], v74 offset:40960
	s_waitcnt lgkmcnt(0)
	v_mfma_f32_32x32x16_bf16 v[52:67], v[78:81], v[82:85], v[52:67]
	ds_read_b64_tr_b16 v[82:83], v73 offset:40960
	ds_read_b64_tr_b16 v[84:85], v72 offset:40960
	s_waitcnt lgkmcnt(0)
	v_mfma_f32_32x32x16_bf16 v[36:51], v[78:81], v[82:85], v[36:51]
	ds_read_b64_tr_b16 v[82:83], v71 offset:40960
	ds_read_b64_tr_b16 v[84:85], v70 offset:40960
	s_waitcnt lgkmcnt(0)
	v_mfma_f32_32x32x16_bf16 v[20:35], v[78:81], v[82:85], v[20:35]
	ds_read_b64_tr_b16 v[82:83], v69 offset:40960
	ds_read_b64_tr_b16 v[84:85], v2 offset:40960
	s_waitcnt lgkmcnt(0)
	v_mfma_f32_32x32x16_bf16 v[4:19], v[78:81], v[82:85], v[4:19]
	ds_read_b64_tr_b16 v[78:79], v77 offset:12288
	ds_read_b64_tr_b16 v[80:81], v75 offset:12288
	ds_read_b64_tr_b16 v[82:83], v76 offset:45056
	ds_read_b64_tr_b16 v[84:85], v74 offset:45056
	s_waitcnt lgkmcnt(0)
	v_mfma_f32_32x32x16_bf16 v[52:67], v[78:81], v[82:85], v[52:67]
	ds_read_b64_tr_b16 v[82:83], v73 offset:45056
	ds_read_b64_tr_b16 v[84:85], v72 offset:45056
	s_waitcnt lgkmcnt(0)
	v_mfma_f32_32x32x16_bf16 v[36:51], v[78:81], v[82:85], v[36:51]
	ds_read_b64_tr_b16 v[82:83], v71 offset:45056
	ds_read_b64_tr_b16 v[84:85], v70 offset:45056
	s_waitcnt lgkmcnt(0)
	v_mfma_f32_32x32x16_bf16 v[20:35], v[78:81], v[82:85], v[20:35]
	ds_read_b64_tr_b16 v[82:83], v69 offset:45056
	ds_read_b64_tr_b16 v[84:85], v2 offset:45056
	s_waitcnt lgkmcnt(0)
	v_mfma_f32_32x32x16_bf16 v[4:19], v[78:81], v[82:85], v[4:19]
	ds_read_b64_tr_b16 v[78:79], v77 offset:16384
	ds_read_b64_tr_b16 v[80:81], v75 offset:16384
	ds_read_b64_tr_b16 v[82:83], v76 offset:49152
	ds_read_b64_tr_b16 v[84:85], v74 offset:49152
	s_waitcnt lgkmcnt(0)
	v_mfma_f32_32x32x16_bf16 v[52:67], v[78:81], v[82:85], v[52:67]
	ds_read_b64_tr_b16 v[82:83], v73 offset:49152
	ds_read_b64_tr_b16 v[84:85], v72 offset:49152
	s_waitcnt lgkmcnt(0)
	v_mfma_f32_32x32x16_bf16 v[36:51], v[78:81], v[82:85], v[36:51]
	ds_read_b64_tr_b16 v[82:83], v71 offset:49152
	ds_read_b64_tr_b16 v[84:85], v70 offset:49152
	s_waitcnt lgkmcnt(0)
	v_mfma_f32_32x32x16_bf16 v[20:35], v[78:81], v[82:85], v[20:35]
	ds_read_b64_tr_b16 v[82:83], v69 offset:49152
	ds_read_b64_tr_b16 v[84:85], v2 offset:49152
	s_waitcnt lgkmcnt(0)
	v_mfma_f32_32x32x16_bf16 v[4:19], v[78:81], v[82:85], v[4:19]
	ds_read_b64_tr_b16 v[78:79], v77 offset:20480
	ds_read_b64_tr_b16 v[80:81], v75 offset:20480
	ds_read_b64_tr_b16 v[82:83], v76 offset:53248
	ds_read_b64_tr_b16 v[84:85], v74 offset:53248
	s_waitcnt lgkmcnt(0)
	v_mfma_f32_32x32x16_bf16 v[52:67], v[78:81], v[82:85], v[52:67]
	ds_read_b64_tr_b16 v[82:83], v73 offset:53248
	ds_read_b64_tr_b16 v[84:85], v72 offset:53248
	s_waitcnt lgkmcnt(0)
	v_mfma_f32_32x32x16_bf16 v[36:51], v[78:81], v[82:85], v[36:51]
	ds_read_b64_tr_b16 v[82:83], v71 offset:53248
	ds_read_b64_tr_b16 v[84:85], v70 offset:53248
	s_waitcnt lgkmcnt(0)
	v_mfma_f32_32x32x16_bf16 v[20:35], v[78:81], v[82:85], v[20:35]
	ds_read_b64_tr_b16 v[82:83], v69 offset:53248
	ds_read_b64_tr_b16 v[84:85], v2 offset:53248
	s_waitcnt lgkmcnt(0)
	v_mfma_f32_32x32x16_bf16 v[4:19], v[78:81], v[82:85], v[4:19]
	ds_read_b64_tr_b16 v[78:79], v77 offset:24576
	ds_read_b64_tr_b16 v[80:81], v75 offset:24576
	ds_read_b64_tr_b16 v[82:83], v76 offset:57344
	ds_read_b64_tr_b16 v[84:85], v74 offset:57344
	s_waitcnt lgkmcnt(0)
	v_mfma_f32_32x32x16_bf16 v[52:67], v[78:81], v[82:85], v[52:67]
	ds_read_b64_tr_b16 v[82:83], v73 offset:57344
	ds_read_b64_tr_b16 v[84:85], v72 offset:57344
	s_waitcnt lgkmcnt(0)
	v_mfma_f32_32x32x16_bf16 v[36:51], v[78:81], v[82:85], v[36:51]
	ds_read_b64_tr_b16 v[82:83], v71 offset:57344
	ds_read_b64_tr_b16 v[84:85], v70 offset:57344
	s_waitcnt lgkmcnt(0)
	v_mfma_f32_32x32x16_bf16 v[20:35], v[78:81], v[82:85], v[20:35]
	ds_read_b64_tr_b16 v[82:83], v69 offset:57344
	ds_read_b64_tr_b16 v[84:85], v2 offset:57344
	s_waitcnt lgkmcnt(0)
	v_mfma_f32_32x32x16_bf16 v[4:19], v[78:81], v[82:85], v[4:19]
	ds_read_b64_tr_b16 v[78:79], v77 offset:28672
	ds_read_b64_tr_b16 v[80:81], v75 offset:28672
	ds_read_b64_tr_b16 v[82:83], v76 offset:61440
	ds_read_b64_tr_b16 v[84:85], v74 offset:61440
	ds_read_b64_tr_b16 v[74:75], v73 offset:61440
	ds_read_b64_tr_b16 v[76:77], v72 offset:61440
	s_waitcnt lgkmcnt(0)
	v_mfma_f32_32x32x16_bf16 v[36:51], v[78:81], v[74:77], v[36:51]
	ds_read_b64_tr_b16 v[72:73], v71 offset:61440
	ds_read_b64_tr_b16 v[74:75], v70 offset:61440
	v_mfma_f32_32x32x16_bf16 v[52:67], v[78:81], v[82:85], v[52:67]
	s_waitcnt lgkmcnt(0)
; #define WG_BAR() do { asm volatile("s_waitcnt vmcnt(0) lgkmcnt(0)" ::: "memory"); __builtin_amdgcn_s_barrier(); asm volatile("" ::: "memory"); } while (0)
; __device__ __forceinline__ int crow(int r, int hi) { return (r & 3) + 8 * (r >> 2) + 4 * hi; }
; __device__ __forceinline__ void retA_unit2(LAS unsigned char* lds, const bf16* proj, const f32x2* rot, float* KV, int uA, int uB, int tid, int lane, int wid) {
;     ...
;     float* kvp = KV + (size_t)u * 16384;
; #pragma unroll
;     for (int k = 0; k < 4; ++k)
; #pragma unroll
;         for (int r = 0; r < 16; ++r) kvp[(32 * db + crow(r, hi)) * 128 + 32 * k + r32] = acc[k][r];
;     WG_BAR();
	v_mfma_f32_32x32x16_bf16 v[20:35], v[78:81], v[72:75], v[20:35]
	ds_read_b64_tr_b16 v[70:71], v69 offset:61440
	ds_read_b64_tr_b16 v[72:73], v2 offset:61440
	v_and_or_b32 v2, v68, 31, s3
	v_lshlrev_b32_e32 v68, 4, v68
	v_and_b32_e32 v68, 0x200, v68
	v_or_b32_e32 v69, v68, v2
	v_lshlrev_b32_e32 v69, 2, v69
	s_nop 2
	global_store_dword v69, v52, s[18:19]
	v_add_lshl_u32 v52, v68, v2, 2
	global_store_dword v52, v53, s[18:19] offset:512
	global_store_dword v52, v54, s[18:19] offset:1024
	global_store_dword v52, v55, s[18:19] offset:1536
	v_or_b32_e32 v53, 0x400, v68
	v_or_b32_e32 v54, v53, v2
	v_lshlrev_b32_e32 v54, 2, v54
	global_store_dword v54, v56, s[18:19]
	v_or_b32_e32 v54, 0x480, v68
	v_or_b32_e32 v55, v54, v2
	v_lshlrev_b32_e32 v55, 2, v55
	global_store_dword v55, v57, s[18:19]
	v_or_b32_e32 v55, 0x500, v68
	v_or_b32_e32 v56, v55, v2
	v_lshlrev_b32_e32 v56, 2, v56
	global_store_dword v56, v58, s[18:19]
	v_or_b32_e32 v56, 0x580, v68
	v_or_b32_e32 v57, v56, v2
	v_lshlrev_b32_e32 v57, 2, v57
	global_store_dword v57, v59, s[18:19]
	v_or_b32_e32 v57, 0x800, v68
	v_or_b32_e32 v58, v57, v2
	v_lshlrev_b32_e32 v58, 2, v58
	global_store_dword v58, v60, s[18:19]
	v_or_b32_e32 v58, 0x880, v68
	v_or_b32_e32 v59, v58, v2
	v_lshlrev_b32_e32 v59, 2, v59
	global_store_dword v59, v61, s[18:19]
	v_or_b32_e32 v59, 0x900, v68
	v_or_b32_e32 v60, v59, v2
	v_lshlrev_b32_e32 v60, 2, v60
	global_store_dword v60, v62, s[18:19]
	v_or_b32_e32 v60, 0x980, v68
	v_or_b32_e32 v61, v60, v2
	v_lshlrev_b32_e32 v61, 2, v61
	global_store_dword v61, v63, s[18:19]
	v_or_b32_e32 v61, 0xc00, v68
	v_or_b32_e32 v62, v61, v2
	v_lshlrev_b32_e32 v62, 2, v62
	global_store_dword v62, v64, s[18:19]
	v_or_b32_e32 v62, 0xc80, v68
	v_or_b32_e32 v63, v62, v2
	v_lshlrev_b32_e32 v63, 2, v63
	global_store_dword v63, v65, s[18:19]
	v_or_b32_e32 v63, 0xd00, v68
	v_or_b32_e32 v64, v63, v2
	v_lshlrev_b32_e32 v64, 2, v64
	global_store_dword v64, v66, s[18:19]
	v_or_b32_e32 v64, 0xd80, v68
	v_or_b32_e32 v65, v64, v2
	v_lshlrev_b32_e32 v65, 2, v65
	global_store_dword v65, v67, s[18:19]
	v_or_b32_e32 v65, 32, v2
	global_store_dword v52, v36, s[18:19] offset:128
	v_add_lshl_u32 v36, v68, v65, 2
	global_store_dword v36, v37, s[18:19] offset:512
	global_store_dword v36, v38, s[18:19] offset:1024
	global_store_dword v36, v39, s[18:19] offset:1536
	v_or_b32_e32 v36, v53, v65
	v_lshlrev_b32_e32 v36, 2, v36
	global_store_dword v36, v40, s[18:19]
	v_or_b32_e32 v36, v54, v65
	v_lshlrev_b32_e32 v36, 2, v36
	global_store_dword v36, v41, s[18:19]
	v_or_b32_e32 v36, v55, v65
	v_lshlrev_b32_e32 v36, 2, v36
	global_store_dword v36, v42, s[18:19]
	v_or_b32_e32 v36, v56, v65
	v_lshlrev_b32_e32 v36, 2, v36
	global_store_dword v36, v43, s[18:19]
	v_or_b32_e32 v36, v57, v65
	v_lshlrev_b32_e32 v36, 2, v36
	global_store_dword v36, v44, s[18:19]
	v_or_b32_e32 v36, v58, v65
	v_lshlrev_b32_e32 v36, 2, v36
	global_store_dword v36, v45, s[18:19]
	v_or_b32_e32 v36, v59, v65
	v_lshlrev_b32_e32 v36, 2, v36
	global_store_dword v36, v46, s[18:19]
	v_or_b32_e32 v36, v60, v65
	v_lshlrev_b32_e32 v36, 2, v36
	global_store_dword v36, v47, s[18:19]
	v_or_b32_e32 v36, v61, v65
	v_lshlrev_b32_e32 v36, 2, v36
	global_store_dword v36, v48, s[18:19]
	v_or_b32_e32 v36, v62, v65
	v_lshlrev_b32_e32 v36, 2, v36
	global_store_dword v36, v49, s[18:19]
	v_or_b32_e32 v36, v63, v65
	v_lshlrev_b32_e32 v36, 2, v36
	global_store_dword v36, v50, s[18:19]
	v_or_b32_e32 v36, v64, v65
	v_lshlrev_b32_e32 v36, 2, v36
	global_store_dword v36, v51, s[18:19]
	v_or_b32_e32 v36, 64, v2
	global_store_dword v52, v20, s[18:19] offset:256
	v_add_lshl_u32 v20, v68, v36, 2
	global_store_dword v20, v21, s[18:19] offset:512
	global_store_dword v20, v22, s[18:19] offset:1024
	global_store_dword v20, v23, s[18:19] offset:1536
	v_or_b32_e32 v20, v53, v36
	v_lshlrev_b32_e32 v20, 2, v20
	global_store_dword v20, v24, s[18:19]
	v_or_b32_e32 v20, v54, v36
	v_lshlrev_b32_e32 v20, 2, v20
	global_store_dword v20, v25, s[18:19]
	v_or_b32_e32 v20, v55, v36
	v_lshlrev_b32_e32 v20, 2, v20
	global_store_dword v20, v26, s[18:19]
	v_or_b32_e32 v20, v56, v36
	v_lshlrev_b32_e32 v20, 2, v20
	global_store_dword v20, v27, s[18:19]
	v_or_b32_e32 v20, v57, v36
	v_lshlrev_b32_e32 v20, 2, v20
	global_store_dword v20, v28, s[18:19]
	v_or_b32_e32 v20, v58, v36
	v_lshlrev_b32_e32 v20, 2, v20
	global_store_dword v20, v29, s[18:19]
	v_or_b32_e32 v20, v59, v36
	v_lshlrev_b32_e32 v20, 2, v20
	global_store_dword v20, v30, s[18:19]
	v_or_b32_e32 v20, v60, v36
	v_lshlrev_b32_e32 v20, 2, v20
	s_waitcnt lgkmcnt(0)
	v_mfma_f32_32x32x16_bf16 v[4:19], v[78:81], v[70:73], v[4:19]
	global_store_dword v20, v31, s[18:19]
	v_or_b32_e32 v20, v61, v36
	v_lshlrev_b32_e32 v20, 2, v20
	global_store_dword v20, v32, s[18:19]
	v_or_b32_e32 v20, v62, v36
	v_lshlrev_b32_e32 v20, 2, v20
	global_store_dword v20, v33, s[18:19]
	v_or_b32_e32 v20, v63, v36
	v_lshlrev_b32_e32 v20, 2, v20
	global_store_dword v20, v34, s[18:19]
	v_or_b32_e32 v20, v64, v36
	v_lshlrev_b32_e32 v20, 2, v20
	v_or_b32_e32 v2, 0x60, v2
	global_store_dword v20, v35, s[18:19]
	global_store_dword v52, v4, s[18:19] offset:384
	v_add_lshl_u32 v4, v68, v2, 2
	global_store_dword v4, v5, s[18:19] offset:512
	global_store_dword v4, v6, s[18:19] offset:1024
	global_store_dword v4, v7, s[18:19] offset:1536
	v_or_b32_e32 v4, v53, v2
	v_lshlrev_b32_e32 v4, 2, v4
	global_store_dword v4, v8, s[18:19]
	v_or_b32_e32 v4, v54, v2
	v_lshlrev_b32_e32 v4, 2, v4
	global_store_dword v4, v9, s[18:19]
	v_or_b32_e32 v4, v55, v2
	v_lshlrev_b32_e32 v4, 2, v4
	global_store_dword v4, v10, s[18:19]
	v_or_b32_e32 v4, v56, v2
	v_lshlrev_b32_e32 v4, 2, v4
	global_store_dword v4, v11, s[18:19]
	v_or_b32_e32 v4, v57, v2
	v_lshlrev_b32_e32 v4, 2, v4
	global_store_dword v4, v12, s[18:19]
	v_or_b32_e32 v4, v58, v2
	v_lshlrev_b32_e32 v4, 2, v4
	global_store_dword v4, v13, s[18:19]
	v_or_b32_e32 v4, v59, v2
	v_lshlrev_b32_e32 v4, 2, v4
	global_store_dword v4, v14, s[18:19]
	v_or_b32_e32 v4, v60, v2
	v_lshlrev_b32_e32 v4, 2, v4
	global_store_dword v4, v15, s[18:19]
	v_or_b32_e32 v4, v61, v2
	v_lshlrev_b32_e32 v4, 2, v4
	global_store_dword v4, v16, s[18:19]
	v_or_b32_e32 v4, v62, v2
	v_lshlrev_b32_e32 v4, 2, v4
	global_store_dword v4, v17, s[18:19]
	v_or_b32_e32 v4, v63, v2
	v_or_b32_e32 v2, v64, v2
	v_lshlrev_b32_e32 v4, 2, v4
	v_lshlrev_b32_e32 v2, 2, v2
	global_store_dword v4, v18, s[18:19]
	global_store_dword v2, v19, s[18:19]
	v_mov_b32_e32 v68, v1
	s_waitcnt vmcnt(0) lgkmcnt(0)
	s_barrier
; #define GAS __attribute__((address_space(1)))
; #define LAS __attribute__((address_space(3)))
; __device__ __forceinline__ unsigned pk2(float lo, float hi) { f32x2_t_ v = {lo, hi}; bf16x2_t_ b = __builtin_convertvector(v, bf16x2_t_); return __builtin_bit_cast(unsigned, b); }
; template <int MODE  > __device__ __forceinline__ void ret_stage_rot(LAS unsigned char* tile, const bf16* src  , const f32x2* rot  , float sc, float l2g, int tid) {
; #pragma unroll
;     for (int i = 0; i < 2; ++i) { const int item = tid + 512 * i, j = item >> 3, cc = item & 7;
;         const v4u lo = *(const GAS v4u*)(src + (size_t)j * LDP + 8 * cc), hh = *(const GAS v4u*)(src + (size_t)j * LDP + 64 + 8 * cc);
;         const GAS f32x4* rp = (const GAS f32x4*)(rot + (size_t)j * 64 + 8 * cc);
;         const f32x4 c0 = rp[0], c1 = rp[1], c2 = rp[2], c3 = rp[3];
;         const float cs[8] = {c0.x, c0.z, c1.x, c1.z, c2.x, c2.z, c3.x, c3.z}, sn[8] = {c0.y, c0.w, c1.y, c1.w, c2.y, c2.w, c3.y, c3.w};
;         const float a[8] = {bflo(lo.x), bfhi(lo.x), bflo(lo.y), bfhi(lo.y), bflo(lo.z), bfhi(lo.z), bflo(lo.w), bfhi(lo.w)};
;         const float bb[8] = {bflo(hh.x), bfhi(hh.x), bflo(hh.y), bfhi(hh.y), bflo(hh.z), bfhi(hh.z), bflo(hh.w), bfhi(hh.w)};
;         const float s = MODE == 1 ? sc * __builtin_amdgcn_exp2f((float)(127 - j) * l2g) : sc;
;         float o1[8], o2[8];
; #pragma unroll
;         for (int e = 0; e < 8; ++e) { o1[e] = (a[e] * cs[e] - bb[e] * sn[e]) * s; o2[e] = (bb[e] * cs[e] + a[e] * sn[e]) * s; }
;         v4u w; w.x = pk2(o1[0], o1[1]); w.y = pk2(o1[2], o1[3]); w.z = pk2(o1[4], o1[5]); w.w = pk2(o1[6], o1[7]); *(LAS v4u*)(tile + offb(j, cc)) = w;
;         w.x = pk2(o2[0], o2[1]); w.y = pk2(o2[2], o2[3]); w.z = pk2(o2[4], o2[5]); w.w = pk2(o2[6], o2[7]); *(LAS v4u*)(tile + offb(j, cc + 8)) = w; }
; __device__ __forceinline__ void retA_unit2(LAS unsigned char* lds, const bf16* proj, const f32x2* rot, float* KV, int uA, int uB, int tid, int lane, int wid) {
;     ...
;     for (int s = 0; s < 2; ++s) { const int u = s ? uB : uA; const int bh = u >> 5, c = u & 31, b = bh >> 3, h = bh & 7; const size_t t0 = (size_t)b * SEQ + c * 128;
;         ret_stage_rot<1>(lds + s * 65536, proj + t0 * LDP + C_KR + h * 128, rot + (size_t)c * 128 * 64, RET_KSCALE, kLog2Gamma[h], tid);
	v_readlane_b32 s18, v252, 42
	v_ashrrev_i32_e32 v38, 3, v68
	v_sub_u32_e32 v6, 0x7f, v38
	v_and_b32_e32 v8, 7, v68
	v_cvt_f32_i32_e32 v61, v6
	v_lshlrev_b32_e32 v6, 2, v38
	v_or_b32_e32 v2, 8, v8
	v_and_b32_e32 v6, 12, v6
	v_bfe_u32 v7, v38, 2, 2
	v_bitop3_b32 v9, v6, v8, v7 bitop3:0x36
	v_bitop3_b32 v6, v6, v2, v7 bitop3:0x36
	v_lshlrev_b32_e32 v59, 4, v6
	v_add_u32_e32 v6, 0x200, v68
	v_ashrrev_i32_e32 v36, 3, v6
	v_sub_u32_e32 v7, 0x7f, v36
	v_cvt_f32_i32_e32 v57, v7
	v_lshlrev_b32_e32 v7, 2, v36
	v_lshlrev_b32_e32 v60, 4, v9
	v_and_b32_e32 v7, 12, v7
	v_bfe_u32 v9, v36, 2, 2
	v_bitop3_b32 v2, v7, v2, v9 bitop3:0x36
	v_ashrrev_i32_e32 v52, 4, v68
	v_lshlrev_b32_e32 v55, 4, v2
	v_lshlrev_b32_e32 v2, 2, v52
	v_bitop3_b32 v10, v7, v8, v9 bitop3:0x36
	v_and_b32_e32 v62, 15, v68
	v_and_b32_e32 v2, 12, v2
	v_bfe_u32 v7, v52, 2, 2
	v_bitop3_b32 v2, v2, v62, v7 bitop3:0x36
	v_ashrrev_i32_e32 v49, 4, v6
	v_lshlrev_b32_e32 v53, 4, v2
	v_lshlrev_b32_e32 v2, 2, v49
	v_and_b32_e32 v2, 12, v2
	v_bfe_u32 v6, v49, 2, 2
	v_bitop3_b32 v2, v2, v62, v6 bitop3:0x36
	v_lshlrev_b32_e32 v50, 4, v2
	v_add_u32_e32 v2, 0x400, v68
	v_ashrrev_i32_e32 v46, 4, v2
	v_lshlrev_b32_e32 v2, 2, v46
	v_and_b32_e32 v2, 12, v2
	v_bfe_u32 v6, v46, 2, 2
	v_bitop3_b32 v2, v2, v62, v6 bitop3:0x36
	v_lshlrev_b32_e32 v48, 4, v2
	v_add_u32_e32 v2, 0x600, v68
	v_ashrrev_i32_e32 v44, 4, v2
	v_lshlrev_b32_e32 v2, 2, v44
	v_readlane_b32 s19, v252, 43
	v_and_b32_e32 v2, 12, v2
	v_bfe_u32 v6, v44, 2, 2
	s_load_dword s0, s[18:19], 0x0
	v_readlane_b32 s18, v252, 40
	v_ashrrev_i32_e32 v39, 31, v38
	v_bitop3_b32 v2, v2, v62, v6 bitop3:0x36
	v_readlane_b32 s19, v252, 41
	v_lshlrev_b64 v[4:5], 9, v[38:39]
	v_lshlrev_b32_e32 v39, 4, v2
	v_lshlrev_b32_e32 v2, 6, v8
	v_mov_b64_e32 v[24:25], s[18:19]
	v_lshl_add_u64 v[22:23], s[24:25], 0, v[2:3]
	v_mad_i64_i32 v[6:7], s[18:19], v38, s33, v[24:25]
	v_lshlrev_b32_e32 v2, 4, v8
	v_lshl_add_u64 v[6:7], v[6:7], 0, v[2:3]
	v_lshl_add_u64 v[16:17], v[22:23], 0, v[4:5]
	v_lshlrev_b32_e32 v56, 4, v10
	s_nop 0
	s_nop 0
	s_waitcnt lgkmcnt(0)
	v_mul_f32_e32 v34, s0, v61
	v_exp_f32_e32 v34, v34
	v_lshlrev_b32_e32 v58, 8, v38
	v_ashrrev_i32_e32 v37, 31, v36
	v_lshlrev_b64 v[20:21], 9, v[36:37]
	v_mul_f32_e32 v34, 0x3db504f3, v34
	v_lshlrev_b32_e32 v54, 8, v36
	v_lshlrev_b32_e32 v51, 8, v52
	v_lshlrev_b32_e32 v47, 8, v49
	v_lshlrev_b32_e32 v45, 8, v46
	v_lshlrev_b32_e32 v37, 8, v44
	s_waitcnt vmcnt(0)
	v_lshlrev_b32_e32 v42, 16, v86
	s_waitcnt vmcnt(0)
	v_lshlrev_b32_e32 v64, 16, v90
	v_and_b32_e32 v65, 0xffff0000, v90
	s_waitcnt vmcnt(0)
	v_mov_b32_e32 v41, v108
	v_mov_b32_e32 v18, v107
	v_and_b32_e32 v43, 0xffff0000, v86
	v_mov_b32_e32 v40, v106
	v_mov_b32_e32 v19, v109
	v_pk_mul_f32 v[16:17], v[18:19], v[64:65]
	v_lshlrev_b32_e32 v30, 16, v91
	v_pk_fma_f32 v[16:17], v[40:41], v[42:43], v[16:17] neg_lo:[0,0,1] neg_hi:[0,0,1]
	v_and_b32_e32 v31, 0xffff0000, v91
	v_pk_mul_f32 v[66:67], v[34:35], v[16:17] op_sel_hi:[0,1]
	v_pk_mul_f32 v[16:17], v[40:41], v[64:65]
	v_lshlrev_b32_e32 v26, 16, v87
	v_pk_fma_f32 v[16:17], v[18:19], v[42:43], v[16:17]
	v_and_b32_e32 v27, 0xffff0000, v87
	v_pk_mul_f32 v[42:43], v[34:35], v[16:17] op_sel_hi:[0,1]
	v_mov_b32_e32 v17, v104
	v_mov_b32_e32 v14, v103
	v_mov_b32_e32 v16, v102
	v_mov_b32_e32 v15, v105
	v_pk_mul_f32 v[12:13], v[14:15], v[30:31]
	v_lshlrev_b32_e32 v70, 16, v92
	v_pk_fma_f32 v[12:13], v[16:17], v[26:27], v[12:13] neg_lo:[0,0,1] neg_hi:[0,0,1]
	v_and_b32_e32 v71, 0xffff0000, v92
	v_pk_mul_f32 v[64:65], v[34:35], v[12:13] op_sel_hi:[0,1]
	v_pk_mul_f32 v[12:13], v[14:15], v[26:27]
	v_lshlrev_b32_e32 v26, 16, v88
	v_pk_fma_f32 v[12:13], v[16:17], v[30:31], v[12:13]
	v_and_b32_e32 v27, 0xffff0000, v88
	v_pk_mul_f32 v[30:31], v[34:35], v[12:13] op_sel_hi:[0,1]
	v_mov_b32_e32 v13, v100
	v_mov_b32_e32 v10, v99
	v_mov_b32_e32 v12, v98
	v_mov_b32_e32 v11, v101
	v_pk_mul_f32 v[8:9], v[10:11], v[70:71]
	v_lshlrev_b32_e32 v28, 16, v93
	v_pk_fma_f32 v[8:9], v[12:13], v[26:27], v[8:9] neg_lo:[0,0,1] neg_hi:[0,0,1]
	s_nop 0
	v_pk_mul_f32 v[72:73], v[34:35], v[8:9] op_sel_hi:[0,1]
	v_pk_mul_f32 v[8:9], v[10:11], v[26:27]
	v_lshlrev_b32_e32 v26, 16, v89
	v_pk_fma_f32 v[8:9], v[12:13], v[70:71], v[8:9]
	v_and_b32_e32 v27, 0xffff0000, v89
	v_pk_mul_f32 v[70:71], v[34:35], v[8:9] op_sel_hi:[0,1]
	v_and_b32_e32 v29, 0xffff0000, v93
	v_mov_b32_e32 v9, v96
	v_mov_b32_e32 v6, v95
	v_mov_b32_e32 v8, v94
	v_mov_b32_e32 v7, v97
	v_pk_mul_f32 v[4:5], v[6:7], v[28:29]
	s_nop 0
	v_pk_fma_f32 v[4:5], v[8:9], v[26:27], v[4:5] neg_lo:[0,0,1] neg_hi:[0,0,1]
	v_pk_mul_f32 v[26:27], v[6:7], v[26:27]
	v_pk_mul_f32 v[4:5], v[34:35], v[4:5] op_sel_hi:[0,1]
	v_pk_fma_f32 v[26:27], v[8:9], v[28:29], v[26:27]
	v_cvt_pk_bf16_f32 v28, v72, v73
	v_pk_mul_f32 v[32:33], v[34:35], v[26:27] op_sel_hi:[0,1]
	v_cvt_pk_bf16_f32 v26, v66, v67
	v_cvt_pk_bf16_f32 v27, v64, v65
	v_cvt_pk_bf16_f32 v29, v4, v5
	v_add3_u32 v4, 0, v60, v58
	ds_write_b128 v4, v[26:29]
	v_cvt_pk_bf16_f32 v26, v42, v43
	v_cvt_pk_bf16_f32 v27, v30, v31
	v_cvt_pk_bf16_f32 v28, v70, v71
	v_cvt_pk_bf16_f32 v29, v32, v33
	v_add3_u32 v4, 0, v59, v58
	ds_write_b128 v4, v[26:29]
	v_mad_i64_i32 v[4:5], s[18:19], v36, s33, v[24:25]
	v_lshl_add_u64 v[4:5], v[4:5], 0, v[2:3]
	v_lshl_add_u64 v[4:5], v[22:23], 0, v[20:21]
	v_mul_f32_e32 v4, s0, v57
	v_exp_f32_e32 v4, v4
	v_readlane_b32 s18, v252, 44
	v_readlane_b32 s19, v252, 45
	v_mul_f32_e32 v4, 0x3db504f3, v4
	s_waitcnt vmcnt(0)
	v_lshlrev_b32_e32 v74, 16, v110
	s_waitcnt vmcnt(0)
	v_lshlrev_b32_e32 v76, 16, v114
	v_and_b32_e32 v77, 0xffff0000, v114
	s_waitcnt vmcnt(0)
; #define GAS __attribute__((address_space(1)))
; #define LAS __attribute__((address_space(3)))
; __device__ __forceinline__ unsigned pk2(float lo, float hi) { f32x2_t_ v = {lo, hi}; bf16x2_t_ b = __builtin_convertvector(v, bf16x2_t_); return __builtin_bit_cast(unsigned, b); }
; template <int MODE  > __device__ __forceinline__ void ret_stage_rot(LAS unsigned char* tile, const bf16* src  , const f32x2* rot  , float sc, float l2g, int tid) {
; #pragma unroll
;     for (int i = 0; i < 2; ++i) { const int item = tid + 512 * i, j = item >> 3, cc = item & 7;
;         const v4u lo = *(const GAS v4u*)(src + (size_t)j * LDP + 8 * cc), hh = *(const GAS v4u*)(src + (size_t)j * LDP + 64 + 8 * cc);
;         const GAS f32x4* rp = (const GAS f32x4*)(rot + (size_t)j * 64 + 8 * cc);
;         const f32x4 c0 = rp[0], c1 = rp[1], c2 = rp[2], c3 = rp[3];
;         const float cs[8] = {c0.x, c0.z, c1.x, c1.z, c2.x, c2.z, c3.x, c3.z}, sn[8] = {c0.y, c0.w, c1.y, c1.w, c2.y, c2.w, c3.y, c3.w};
;         const float a[8] = {bflo(lo.x), bfhi(lo.x), bflo(lo.y), bfhi(lo.y), bflo(lo.z), bfhi(lo.z), bflo(lo.w), bfhi(lo.w)};
;         const float bb[8] = {bflo(hh.x), bfhi(hh.x), bflo(hh.y), bfhi(hh.y), bflo(hh.z), bfhi(hh.z), bflo(hh.w), bfhi(hh.w)};
;         const float s = MODE == 1 ? sc * __builtin_amdgcn_exp2f((float)(127 - j) * l2g) : sc;
;         float o1[8], o2[8];
; #pragma unroll
;         for (int e = 0; e < 8; ++e) { o1[e] = (a[e] * cs[e] - bb[e] * sn[e]) * s; o2[e] = (bb[e] * cs[e] + a[e] * sn[e]) * s; }
;         v4u w; w.x = pk2(o1[0], o1[1]); w.y = pk2(o1[2], o1[3]); w.z = pk2(o1[4], o1[5]); w.w = pk2(o1[6], o1[7]); *(LAS v4u*)(tile + offb(j, cc)) = w;
;         w.x = pk2(o2[0], o2[1]); w.y = pk2(o2[2], o2[3]); w.z = pk2(o2[4], o2[5]); w.w = pk2(o2[6], o2[7]); *(LAS v4u*)(tile + offb(j, cc + 8)) = w; }
; }
; __device__ __forceinline__ void ret_stage_plain(LAS unsigned char* tile, const bf16* src, int ld, int tid) {
; #pragma unroll
;     for (int i = 0; i < 4; ++i) { const int item = tid + 512 * i, row = item >> 4, ch = item & 15; *(LAS v4u*)(tile + offb(row, ch)) = *(const GAS v4u*)(src + (size_t)row * ld + 8 * ch); }
; }
	v_mov_b32_e32 v43, v132
	v_mov_b32_e32 v34, v131
	v_and_b32_e32 v75, 0xffff0000, v110
	v_mov_b32_e32 v42, v130
	v_mov_b32_e32 v35, v133
	v_pk_mul_f32 v[32:33], v[34:35], v[76:77]
	v_lshlrev_b32_e32 v70, 16, v115
	v_pk_fma_f32 v[32:33], v[42:43], v[74:75], v[32:33] neg_lo:[0,0,1] neg_hi:[0,0,1]
	v_and_b32_e32 v71, 0xffff0000, v115
	v_pk_mul_f32 v[78:79], v[4:5], v[32:33] op_sel_hi:[0,1]
	v_pk_mul_f32 v[32:33], v[42:43], v[76:77]
	v_lshlrev_b32_e32 v64, 16, v111
	v_pk_fma_f32 v[32:33], v[34:35], v[74:75], v[32:33]
	v_and_b32_e32 v65, 0xffff0000, v111
	v_pk_mul_f32 v[74:75], v[4:5], v[32:33] op_sel_hi:[0,1]
	v_mov_b32_e32 v33, v128
	v_mov_b32_e32 v30, v127
	v_mov_b32_e32 v32, v126
	v_mov_b32_e32 v31, v129
	v_pk_mul_f32 v[28:29], v[30:31], v[70:71]
	v_lshlrev_b32_e32 v80, 16, v116
	v_pk_fma_f32 v[28:29], v[32:33], v[64:65], v[28:29] neg_lo:[0,0,1] neg_hi:[0,0,1]
	v_and_b32_e32 v81, 0xffff0000, v116
	v_pk_mul_f32 v[76:77], v[4:5], v[28:29] op_sel_hi:[0,1]
	v_pk_mul_f32 v[28:29], v[30:31], v[64:65]
	v_lshlrev_b32_e32 v64, 16, v112
	v_pk_fma_f32 v[28:29], v[32:33], v[70:71], v[28:29]
	v_and_b32_e32 v65, 0xffff0000, v112
	v_pk_mul_f32 v[70:71], v[4:5], v[28:29] op_sel_hi:[0,1]
	v_mov_b32_e32 v29, v124
	v_mov_b32_e32 v26, v123
	v_mov_b32_e32 v28, v122
	v_mov_b32_e32 v27, v125
	v_pk_mul_f32 v[24:25], v[26:27], v[80:81]
	v_lshlrev_b32_e32 v66, 16, v117
	v_pk_fma_f32 v[24:25], v[28:29], v[64:65], v[24:25] neg_lo:[0,0,1] neg_hi:[0,0,1]
	s_nop 0
	v_pk_mul_f32 v[82:83], v[4:5], v[24:25] op_sel_hi:[0,1]
	v_pk_mul_f32 v[24:25], v[26:27], v[64:65]
	v_lshlrev_b32_e32 v64, 16, v113
	v_pk_fma_f32 v[24:25], v[28:29], v[80:81], v[24:25]
	v_and_b32_e32 v65, 0xffff0000, v113
	v_pk_mul_f32 v[80:81], v[4:5], v[24:25] op_sel_hi:[0,1]
	v_and_b32_e32 v67, 0xffff0000, v117
	v_mov_b32_e32 v25, v120
	v_mov_b32_e32 v22, v119
	v_mov_b32_e32 v24, v118
	v_mov_b32_e32 v23, v121
	v_pk_mul_f32 v[20:21], v[22:23], v[66:67]
	s_nop 0
	v_pk_fma_f32 v[20:21], v[24:25], v[64:65], v[20:21] neg_lo:[0,0,1] neg_hi:[0,0,1]
	v_pk_mul_f32 v[64:65], v[22:23], v[64:65]
	v_pk_mul_f32 v[20:21], v[4:5], v[20:21] op_sel_hi:[0,1]
	v_pk_fma_f32 v[64:65], v[24:25], v[66:67], v[64:65]
	v_cvt_pk_bf16_f32 v66, v82, v83
	v_pk_mul_f32 v[4:5], v[4:5], v[64:65] op_sel_hi:[0,1]
	v_cvt_pk_bf16_f32 v64, v78, v79
	v_cvt_pk_bf16_f32 v65, v76, v77
	v_cvt_pk_bf16_f32 v67, v20, v21
	v_add3_u32 v20, 0, v56, v54
	ds_write_b128 v20, v[64:67]
	v_cvt_pk_bf16_f32 v64, v74, v75
	v_cvt_pk_bf16_f32 v65, v70, v71
	v_cvt_pk_bf16_f32 v66, v80, v81
	v_cvt_pk_bf16_f32 v67, v4, v5
	v_add3_u32 v4, 0, v55, v54
	ds_write_b128 v4, v[64:67]
	v_lshlrev_b32_e32 v4, 4, v62
	v_mov_b32_e32 v5, v3
	v_lshl_add_u64 v[20:21], s[18:19], 0, v[4:5]
	v_mad_i64_i32 v[62:63], s[18:19], v52, s33, v[20:21]
	v_add3_u32 v66, 0, v53, v51
	s_waitcnt vmcnt(0)
	ds_write_b128 v66, v[134:137] offset:32768
	v_mad_i64_i32 v[62:63], s[18:19], v49, s33, v[20:21]
	v_add3_u32 v66, 0, v50, v47
	s_waitcnt vmcnt(0)
	ds_write_b128 v66, v[138:141] offset:32768
	v_mad_i64_i32 v[62:63], s[18:19], v46, s33, v[20:21]
	v_add3_u32 v66, 0, v48, v45
	v_mad_i64_i32 v[20:21], s[18:19], v44, s33, v[20:21]
	v_readlane_b32 s18, v252, 50
	v_readlane_b32 s19, v252, 51
	s_load_dword s0, s[18:19], 0x0
	v_readlane_b32 s18, v252, 48
	v_readlane_b32 s19, v252, 49
	s_waitcnt vmcnt(0)
	ds_write_b128 v66, v[142:145] offset:32768
	v_add3_u32 v20, 0, v39, v37
	s_waitcnt vmcnt(0)
	ds_write_b128 v20, v[146:149] offset:32768
	v_mov_b64_e32 v[20:21], s[18:19]
	v_mad_i64_i32 v[62:63], s[18:19], v38, s33, v[20:21]
	v_lshl_add_u64 v[66:67], v[62:63], 0, v[2:3]
	s_waitcnt lgkmcnt(0)
	v_mul_f32_e32 v38, s0, v61
	v_exp_f32_e32 v38, v38
	s_waitcnt vmcnt(0)
	v_lshlrev_b32_e32 v66, 16, v150
	s_waitcnt vmcnt(0)
	v_lshlrev_b32_e32 v74, 16, v154
	v_and_b32_e32 v75, 0xffff0000, v154
	v_and_b32_e32 v67, 0xffff0000, v150
	v_pk_mul_f32 v[76:77], v[18:19], v[74:75]
	v_lshlrev_b32_e32 v62, 16, v155
	v_pk_fma_f32 v[76:77], v[40:41], v[66:67], v[76:77] neg_lo:[0,0,1] neg_hi:[0,0,1]
	v_pk_mul_f32 v[40:41], v[40:41], v[74:75]
	v_mul_f32_e32 v38, 0x3db504f3, v38
	v_pk_fma_f32 v[18:19], v[18:19], v[66:67], v[40:41]
	v_lshlrev_b32_e32 v40, 16, v151
	v_and_b32_e32 v41, 0xffff0000, v151
	v_and_b32_e32 v63, 0xffff0000, v155
	v_pk_mul_f32 v[66:67], v[14:15], v[62:63]
	v_pk_mul_f32 v[76:77], v[38:39], v[76:77] op_sel_hi:[0,1]
	v_pk_fma_f32 v[66:67], v[16:17], v[40:41], v[66:67] neg_lo:[0,0,1] neg_hi:[0,0,1]
	v_pk_mul_f32 v[16:17], v[16:17], v[62:63]
	v_pk_mul_f32 v[66:67], v[38:39], v[66:67] op_sel_hi:[0,1]
	v_pk_fma_f32 v[14:15], v[14:15], v[40:41], v[16:17]
	v_lshlrev_b32_e32 v40, 16, v156
	v_and_b32_e32 v41, 0xffff0000, v156
	v_lshlrev_b32_e32 v16, 16, v152
	v_and_b32_e32 v17, 0xffff0000, v152
	v_pk_mul_f32 v[62:63], v[10:11], v[40:41]
	v_pk_mul_f32 v[18:19], v[38:39], v[18:19] op_sel_hi:[0,1]
	v_pk_fma_f32 v[62:63], v[12:13], v[16:17], v[62:63] neg_lo:[0,0,1] neg_hi:[0,0,1]
	v_pk_mul_f32 v[12:13], v[12:13], v[40:41]
	v_pk_mul_f32 v[62:63], v[38:39], v[62:63] op_sel_hi:[0,1]
	v_pk_fma_f32 v[10:11], v[10:11], v[16:17], v[12:13]
	v_lshlrev_b32_e32 v16, 16, v157
	v_and_b32_e32 v17, 0xffff0000, v157
	v_lshlrev_b32_e32 v12, 16, v153
	v_and_b32_e32 v13, 0xffff0000, v153
	v_pk_mul_f32 v[40:41], v[6:7], v[16:17]
	v_pk_mul_f32 v[14:15], v[38:39], v[14:15] op_sel_hi:[0,1]
	v_pk_fma_f32 v[40:41], v[8:9], v[12:13], v[40:41] neg_lo:[0,0,1] neg_hi:[0,0,1]
	v_pk_mul_f32 v[8:9], v[8:9], v[16:17]
	v_pk_mul_f32 v[40:41], v[38:39], v[40:41] op_sel_hi:[0,1]
	v_pk_fma_f32 v[6:7], v[6:7], v[12:13], v[8:9]
	v_pk_mul_f32 v[10:11], v[38:39], v[10:11] op_sel_hi:[0,1]
	v_pk_mul_f32 v[12:13], v[38:39], v[6:7] op_sel_hi:[0,1]
	v_cvt_pk_bf16_f32 v6, v76, v77
	v_cvt_pk_bf16_f32 v7, v66, v67
	v_cvt_pk_bf16_f32 v8, v62, v63
	v_cvt_pk_bf16_f32 v9, v40, v41
	v_add3_u32 v16, s4, v60, v58
	ds_write_b128 v16, v[6:9]
	v_cvt_pk_bf16_f32 v6, v18, v19
	v_cvt_pk_bf16_f32 v7, v14, v15
	v_cvt_pk_bf16_f32 v8, v10, v11
	v_cvt_pk_bf16_f32 v9, v12, v13
	v_add3_u32 v10, s4, v59, v58
	ds_write_b128 v10, v[6:9]
	v_mad_i64_i32 v[6:7], s[18:19], v36, s33, v[20:21]
	v_lshl_add_u64 v[10:11], v[6:7], 0, v[2:3]
	s_nop 0
	v_mul_f32_e32 v2, s0, v57
	v_exp_f32_e32 v2, v2
	v_readlane_b32 s18, v252, 54
	v_readlane_b32 s19, v252, 55
	v_mul_f32_e32 v2, 0x3db504f3, v2
	s_waitcnt vmcnt(0)
; #define GAS __attribute__((address_space(1)))
; #define LAS __attribute__((address_space(3)))
; #define WG_BAR() do { asm volatile("s_waitcnt vmcnt(0) lgkmcnt(0)" ::: "memory"); __builtin_amdgcn_s_barrier(); asm volatile("" ::: "memory"); } while (0)
; __device__ __forceinline__ unsigned tr_off(int lane, int c, int t) { const int h = lane >> 5, blk = (lane >> 4) & 1, q = (lane & 15) >> 2, p = lane & 3; return offb(8 * h + 4 * t + q, 4 * c + 2 * blk + (p >> 1)) + 8u * (unsigned)(p & 1); }
; __device__ __forceinline__ bf16x8 trfrag(LAS unsigned char* tile, unsigned o0, unsigned o1) { const s16x4 a = ldtr(tile + o0), b = ldtr(tile + o1); return (bf16x8){a[0], a[1], a[2], a[3], b[0], b[1], b[2], b[3]}; }
; #define MFMA32(a, b, c) __builtin_amdgcn_mfma_f32_32x32x16_bf16((a), (b), (c), 0, 0, 0)
; __device__ __forceinline__ void ret_stage_plain(LAS unsigned char* tile, const bf16* src, int ld, int tid) {
; #pragma unroll
;     for (int i = 0; i < 4; ++i) { const int item = tid + 512 * i, row = item >> 4, ch = item & 15; *(LAS v4u*)(tile + offb(row, ch)) = *(const GAS v4u*)(src + (size_t)row * ld + 8 * ch); }
; }
; __device__ __forceinline__ void retA_unit2(LAS unsigned char* lds, const bf16* proj, const f32x2* rot, float* KV, int uA, int uB, int tid, int lane, int wid) {
;     ...
;     WG_BAR();
;     const int half = wid >> 2, db = wid & 3, u = half ? uB : uA;
;     LAS unsigned char* base = lds + half * 65536;
;     const unsigned a0 = tr_off(lane, db, 0), a1 = tr_off(lane, db, 1);
;     unsigned b0[4], b1[4];
; #pragma unroll
;     for (int k = 0; k < 4; ++k) { b0[k] = 32768u + tr_off(lane, k, 0); b1[k] = 32768u + tr_off(lane, k, 1); }
;     f32x16 acc[4] = {splat16(0.f), splat16(0.f), splat16(0.f), splat16(0.f)};
; #pragma unroll
;     for (int ks = 0; ks < 8; ++ks) { const bf16x8 A = trfrag(base, a0 + 4096u * ks, a1 + 4096u * ks);
; #pragma unroll
;         for (int k = 0; k < 4; ++k) { const bf16x8 B = trfrag(base, b0[k] + 4096u * ks, b1[k] + 4096u * ks); acc[k] = MFMA32(A, B, acc[k]); } }
	v_lshlrev_b32_e32 v14, 16, v158
	s_waitcnt vmcnt(0)
	v_lshlrev_b32_e32 v16, 16, v162
	v_and_b32_e32 v17, 0xffff0000, v162
	v_and_b32_e32 v15, 0xffff0000, v158
	v_pk_mul_f32 v[18:19], v[34:35], v[16:17]
	v_pk_mul_f32 v[16:17], v[42:43], v[16:17]
	v_lshlrev_b32_e32 v10, 16, v163
	v_and_b32_e32 v11, 0xffff0000, v163
	v_pk_fma_f32 v[18:19], v[42:43], v[14:15], v[18:19] neg_lo:[0,0,1] neg_hi:[0,0,1]
	v_pk_fma_f32 v[14:15], v[34:35], v[14:15], v[16:17]
	v_lshlrev_b32_e32 v6, 16, v159
	v_and_b32_e32 v7, 0xffff0000, v159
	v_pk_mul_f32 v[16:17], v[30:31], v[10:11]
	v_pk_mul_f32 v[10:11], v[32:33], v[10:11]
	v_pk_fma_f32 v[16:17], v[32:33], v[6:7], v[16:17] neg_lo:[0,0,1] neg_hi:[0,0,1]
	v_pk_fma_f32 v[6:7], v[30:31], v[6:7], v[10:11]
	v_lshlrev_b32_e32 v20, 16, v164
	v_and_b32_e32 v21, 0xffff0000, v164
	v_pk_mul_f32 v[10:11], v[2:3], v[6:7] op_sel_hi:[0,1]
	v_lshlrev_b32_e32 v6, 16, v160
	v_and_b32_e32 v7, 0xffff0000, v160
	v_pk_mul_f32 v[30:31], v[26:27], v[20:21]
	v_pk_mul_f32 v[20:21], v[28:29], v[20:21]
	v_pk_fma_f32 v[30:31], v[28:29], v[6:7], v[30:31] neg_lo:[0,0,1] neg_hi:[0,0,1]
	v_pk_fma_f32 v[6:7], v[26:27], v[6:7], v[20:21]
	v_lshlrev_b32_e32 v8, 16, v165
	v_pk_mul_f32 v[20:21], v[2:3], v[6:7] op_sel_hi:[0,1]
	v_lshlrev_b32_e32 v6, 16, v161
	v_and_b32_e32 v7, 0xffff0000, v161
	v_and_b32_e32 v9, 0xffff0000, v165
	v_pk_mul_f32 v[12:13], v[22:23], v[8:9]
	v_pk_mul_f32 v[8:9], v[24:25], v[8:9]
	v_pk_fma_f32 v[12:13], v[24:25], v[6:7], v[12:13] neg_lo:[0,0,1] neg_hi:[0,0,1]
	v_pk_mul_f32 v[18:19], v[2:3], v[18:19] op_sel_hi:[0,1]
	v_pk_mul_f32 v[16:17], v[2:3], v[16:17] op_sel_hi:[0,1]
	v_pk_mul_f32 v[30:31], v[2:3], v[30:31] op_sel_hi:[0,1]
	v_pk_mul_f32 v[12:13], v[2:3], v[12:13] op_sel_hi:[0,1]
	v_pk_fma_f32 v[6:7], v[22:23], v[6:7], v[8:9]
	v_pk_mul_f32 v[14:15], v[2:3], v[14:15] op_sel_hi:[0,1]
	v_pk_mul_f32 v[22:23], v[2:3], v[6:7] op_sel_hi:[0,1]
	v_cvt_pk_bf16_f32 v6, v18, v19
	v_cvt_pk_bf16_f32 v7, v16, v17
	v_cvt_pk_bf16_f32 v8, v30, v31
	v_cvt_pk_bf16_f32 v9, v12, v13
	v_add3_u32 v2, s4, v56, v54
	ds_write_b128 v2, v[6:9]
	v_cvt_pk_bf16_f32 v6, v14, v15
	v_cvt_pk_bf16_f32 v7, v10, v11
	v_cvt_pk_bf16_f32 v8, v20, v21
	v_cvt_pk_bf16_f32 v9, v22, v23
	v_add3_u32 v2, s4, v55, v54
	ds_write_b128 v2, v[6:9]
	v_lshl_add_u64 v[8:9], s[18:19], 0, v[4:5]
	v_mad_i64_i32 v[4:5], s[18:19], v52, s33, v[8:9]
	v_add3_u32 v2, s5, v53, v51
	v_lshlrev_b32_e32 v11, 3, v68
	v_and_b32_e32 v11, 8, v11
	s_waitcnt vmcnt(0)
	ds_write_b128 v2, v[166:169]
	v_mad_i64_i32 v[4:5], s[18:19], v49, s33, v[8:9]
	v_add3_u32 v2, s5, v50, v47
	s_waitcnt vmcnt(0)
	ds_write_b128 v2, v[170:173]
	v_mad_i64_i32 v[4:5], s[18:19], v46, s33, v[8:9]
	v_add3_u32 v2, s5, v48, v45
	s_waitcnt vmcnt(0)
	ds_write_b128 v2, v[174:177]
	v_mad_i64_i32 v[4:5], s[18:19], v44, s33, v[8:9]
	v_add3_u32 v2, s5, v39, v37
	v_readlane_b32 s4, v252, 56
	v_readlane_b32 s5, v252, 57
	s_waitcnt vmcnt(0)
	ds_write_b128 v2, v[178:181]
	v_lshrrev_b32_e32 v2, 2, v68
	v_lshrrev_b32_e32 v4, 3, v68
	v_and_b32_e32 v2, 11, v2
	v_and_b32_e32 v4, 2, v4
	v_lshrrev_b32_e32 v5, 1, v68
	v_and_or_b32 v4, v5, 1, v4
	v_lshlrev_b32_e32 v6, 8, v2
	v_lshrrev_b32_e32 v8, 2, v2
	v_or_b32_e32 v2, 4, v2
	v_or_b32_e32 v5, s95, v4
	v_and_b32_e32 v7, 12, v68
	v_lshlrev_b32_e32 v12, 8, v2
	v_lshrrev_b32_e32 v2, 2, v2
	v_or_b32_e32 v9, v8, v7
	v_bitop3_b32 v10, v8, v5, v7 bitop3:0x36
	v_or_b32_e32 v13, v11, v6
	v_or_b32_e32 v14, v11, v12
	v_bitop3_b32 v8, v8, v4, v7 bitop3:0x36
	v_bitop3_b32 v15, v2, v4, v7 bitop3:0x36
	v_bitop3_b32 v5, v2, v5, v7 bitop3:0x36
	v_or_b32_e32 v16, 4, v4
	v_bitop3_b32 v17, v4, v9, 4 bitop3:0x36
	v_or_b32_e32 v18, 8, v4
	v_bitop3_b32 v19, v4, v9, 8 bitop3:0x36
	v_or_b32_e32 v20, 12, v4
	v_bitop3_b32 v69, v4, v9, 12 bitop3:0x36
	v_lshl_add_u32 v4, v10, 4, s51
	v_lshl_or_b32 v8, v8, 4, v13
	v_lshl_or_b32 v10, v15, 4, v14
	s_waitcnt vmcnt(0) lgkmcnt(0)
	v_mov_b32_e32 v64, v152
	v_mov_b32_e32 v65, v153
	v_mov_b32_e32 v70, v154
	v_mov_b32_e32 v71, v155
	v_mov_b32_e32 v72, v156
	v_mov_b32_e32 v73, v157
	s_barrier
	v_add3_u32 v77, v4, v6, v11
	v_lshl_add_u32 v4, v5, 4, s51
	v_add_u32_e32 v76, s51, v8
	v_add_u32_e32 v74, s51, v10
	v_bitop3_b32 v16, v2, v16, v7 bitop3:0x36
	v_bitop3_b32 v18, v2, v18, v7 bitop3:0x36
	v_bitop3_b32 v2, v2, v20, v7 bitop3:0x36
	v_add3_u32 v75, v4, v12, v11
	ds_read_b64_tr_b16 v[4:5], v77
	ds_read_b64_tr_b16 v[6:7], v75
	ds_read_b64_tr_b16 v[8:9], v76 offset:32768
	ds_read_b64_tr_b16 v[10:11], v74 offset:32768
	s_waitcnt lgkmcnt(0)
	v_mfma_f32_32x32x16_bf16 v[52:67], v[4:7], v[8:11], 0
	v_lshl_or_b32 v8, v17, 4, v13
	v_lshl_or_b32 v10, v16, 4, v14
	v_add_u32_e32 v73, s51, v8
	v_add_u32_e32 v72, s51, v10
	ds_read_b64_tr_b16 v[8:9], v73 offset:32768
	ds_read_b64_tr_b16 v[10:11], v72 offset:32768
	v_lshl_or_b32 v2, v2, 4, v14
	s_waitcnt lgkmcnt(0)
	v_mfma_f32_32x32x16_bf16 v[36:51], v[4:7], v[8:11], 0
	v_lshl_or_b32 v8, v19, 4, v13
	v_lshl_or_b32 v10, v18, 4, v14
	v_add_u32_e32 v71, s51, v8
	v_add_u32_e32 v70, s51, v10
	ds_read_b64_tr_b16 v[8:9], v71 offset:32768
	ds_read_b64_tr_b16 v[10:11], v70 offset:32768
	v_add_u32_e32 v2, s51, v2
	s_waitcnt lgkmcnt(0)
	v_mfma_f32_32x32x16_bf16 v[20:35], v[4:7], v[8:11], 0
	v_lshl_or_b32 v8, v69, 4, v13
	v_add_u32_e32 v69, s51, v8
	ds_read_b64_tr_b16 v[8:9], v69 offset:32768
	ds_read_b64_tr_b16 v[10:11], v2 offset:32768
	ds_read_b64_tr_b16 v[78:79], v77 offset:4096
	ds_read_b64_tr_b16 v[80:81], v75 offset:4096
	ds_read_b64_tr_b16 v[82:83], v76 offset:36864
	ds_read_b64_tr_b16 v[84:85], v74 offset:36864
	s_waitcnt lgkmcnt(0)
	v_mfma_f32_32x32x16_bf16 v[52:67], v[78:81], v[82:85], v[52:67]
	ds_read_b64_tr_b16 v[82:83], v73 offset:36864
	ds_read_b64_tr_b16 v[84:85], v72 offset:36864
	s_waitcnt lgkmcnt(0)
; __device__ __forceinline__ bf16x8 trfrag(LAS unsigned char* tile, unsigned o0, unsigned o1) { const s16x4 a = ldtr(tile + o0), b = ldtr(tile + o1); return (bf16x8){a[0], a[1], a[2], a[3], b[0], b[1], b[2], b[3]}; }
; #define MFMA32(a, b, c) __builtin_amdgcn_mfma_f32_32x32x16_bf16((a), (b), (c), 0, 0, 0)
; __device__ __forceinline__ void retA_unit2(LAS unsigned char* lds, const bf16* proj, const f32x2* rot, float* KV, int uA, int uB, int tid, int lane, int wid) {
;     ...
; #pragma unroll
;     for (int ks = 0; ks < 8; ++ks) { const bf16x8 A = trfrag(base, a0 + 4096u * ks, a1 + 4096u * ks);
; #pragma unroll
;         for (int k = 0; k < 4; ++k) { const bf16x8 B = trfrag(base, b0[k] + 4096u * ks, b1[k] + 4096u * ks); acc[k] = MFMA32(A, B, acc[k]); } }
	v_mfma_f32_32x32x16_bf16 v[36:51], v[78:81], v[82:85], v[36:51]
	ds_read_b64_tr_b16 v[82:83], v71 offset:36864
	ds_read_b64_tr_b16 v[84:85], v70 offset:36864
	v_mfma_f32_32x32x16_bf16 v[4:19], v[4:7], v[8:11], 0
	s_waitcnt lgkmcnt(0)
	v_mfma_f32_32x32x16_bf16 v[20:35], v[78:81], v[82:85], v[20:35]
	ds_read_b64_tr_b16 v[82:83], v69 offset:36864
	ds_read_b64_tr_b16 v[84:85], v2 offset:36864
	s_waitcnt lgkmcnt(0)
	v_mfma_f32_32x32x16_bf16 v[4:19], v[78:81], v[82:85], v[4:19]
	ds_read_b64_tr_b16 v[78:79], v77 offset:8192
	ds_read_b64_tr_b16 v[80:81], v75 offset:8192
	ds_read_b64_tr_b16 v[82:83], v76 offset:40960
	ds_read_b64_tr_b16 v[84:85], v74 offset:40960
	s_waitcnt lgkmcnt(0)
	v_mfma_f32_32x32x16_bf16 v[52:67], v[78:81], v[82:85], v[52:67]
	ds_read_b64_tr_b16 v[82:83], v73 offset:40960
	ds_read_b64_tr_b16 v[84:85], v72 offset:40960
	s_waitcnt lgkmcnt(0)
	v_mfma_f32_32x32x16_bf16 v[36:51], v[78:81], v[82:85], v[36:51]
	ds_read_b64_tr_b16 v[82:83], v71 offset:40960
	ds_read_b64_tr_b16 v[84:85], v70 offset:40960
	s_waitcnt lgkmcnt(0)
	v_mfma_f32_32x32x16_bf16 v[20:35], v[78:81], v[82:85], v[20:35]
	ds_read_b64_tr_b16 v[82:83], v69 offset:40960
	ds_read_b64_tr_b16 v[84:85], v2 offset:40960
	s_waitcnt lgkmcnt(0)
	v_mfma_f32_32x32x16_bf16 v[4:19], v[78:81], v[82:85], v[4:19]
	ds_read_b64_tr_b16 v[78:79], v77 offset:12288
	ds_read_b64_tr_b16 v[80:81], v75 offset:12288
	ds_read_b64_tr_b16 v[82:83], v76 offset:45056
	ds_read_b64_tr_b16 v[84:85], v74 offset:45056
	s_waitcnt lgkmcnt(0)
	v_mfma_f32_32x32x16_bf16 v[52:67], v[78:81], v[82:85], v[52:67]
	ds_read_b64_tr_b16 v[82:83], v73 offset:45056
	ds_read_b64_tr_b16 v[84:85], v72 offset:45056
	s_waitcnt lgkmcnt(0)
	v_mfma_f32_32x32x16_bf16 v[36:51], v[78:81], v[82:85], v[36:51]
	ds_read_b64_tr_b16 v[82:83], v71 offset:45056
	ds_read_b64_tr_b16 v[84:85], v70 offset:45056
	s_waitcnt lgkmcnt(0)
	v_mfma_f32_32x32x16_bf16 v[20:35], v[78:81], v[82:85], v[20:35]
	ds_read_b64_tr_b16 v[82:83], v69 offset:45056
	ds_read_b64_tr_b16 v[84:85], v2 offset:45056
	s_waitcnt lgkmcnt(0)
	v_mfma_f32_32x32x16_bf16 v[4:19], v[78:81], v[82:85], v[4:19]
	ds_read_b64_tr_b16 v[78:79], v77 offset:16384
	ds_read_b64_tr_b16 v[80:81], v75 offset:16384
	ds_read_b64_tr_b16 v[82:83], v76 offset:49152
	ds_read_b64_tr_b16 v[84:85], v74 offset:49152
	s_waitcnt lgkmcnt(0)
	v_mfma_f32_32x32x16_bf16 v[52:67], v[78:81], v[82:85], v[52:67]
	ds_read_b64_tr_b16 v[82:83], v73 offset:49152
	ds_read_b64_tr_b16 v[84:85], v72 offset:49152
	s_waitcnt lgkmcnt(0)
	v_mfma_f32_32x32x16_bf16 v[36:51], v[78:81], v[82:85], v[36:51]
	ds_read_b64_tr_b16 v[82:83], v71 offset:49152
	ds_read_b64_tr_b16 v[84:85], v70 offset:49152
	s_waitcnt lgkmcnt(0)
	v_mfma_f32_32x32x16_bf16 v[20:35], v[78:81], v[82:85], v[20:35]
	ds_read_b64_tr_b16 v[82:83], v69 offset:49152
	ds_read_b64_tr_b16 v[84:85], v2 offset:49152
	s_waitcnt lgkmcnt(0)
	v_mfma_f32_32x32x16_bf16 v[4:19], v[78:81], v[82:85], v[4:19]
	ds_read_b64_tr_b16 v[78:79], v77 offset:20480
	ds_read_b64_tr_b16 v[80:81], v75 offset:20480
	ds_read_b64_tr_b16 v[82:83], v76 offset:53248
	ds_read_b64_tr_b16 v[84:85], v74 offset:53248
	s_waitcnt lgkmcnt(0)
	v_mfma_f32_32x32x16_bf16 v[52:67], v[78:81], v[82:85], v[52:67]
	ds_read_b64_tr_b16 v[82:83], v73 offset:53248
	ds_read_b64_tr_b16 v[84:85], v72 offset:53248
	s_waitcnt lgkmcnt(0)
	v_mfma_f32_32x32x16_bf16 v[36:51], v[78:81], v[82:85], v[36:51]
	ds_read_b64_tr_b16 v[82:83], v71 offset:53248
	ds_read_b64_tr_b16 v[84:85], v70 offset:53248
	s_waitcnt lgkmcnt(0)
	v_mfma_f32_32x32x16_bf16 v[20:35], v[78:81], v[82:85], v[20:35]
	ds_read_b64_tr_b16 v[82:83], v69 offset:53248
	ds_read_b64_tr_b16 v[84:85], v2 offset:53248
	s_waitcnt lgkmcnt(0)
	v_mfma_f32_32x32x16_bf16 v[4:19], v[78:81], v[82:85], v[4:19]
	ds_read_b64_tr_b16 v[78:79], v77 offset:24576
	ds_read_b64_tr_b16 v[80:81], v75 offset:24576
	ds_read_b64_tr_b16 v[82:83], v76 offset:57344
	ds_read_b64_tr_b16 v[84:85], v74 offset:57344
	s_waitcnt lgkmcnt(0)
	v_mfma_f32_32x32x16_bf16 v[52:67], v[78:81], v[82:85], v[52:67]
	ds_read_b64_tr_b16 v[82:83], v73 offset:57344
	ds_read_b64_tr_b16 v[84:85], v72 offset:57344
	s_waitcnt lgkmcnt(0)
	v_mfma_f32_32x32x16_bf16 v[36:51], v[78:81], v[82:85], v[36:51]
	ds_read_b64_tr_b16 v[82:83], v71 offset:57344
	ds_read_b64_tr_b16 v[84:85], v70 offset:57344
	s_waitcnt lgkmcnt(0)
	v_mfma_f32_32x32x16_bf16 v[20:35], v[78:81], v[82:85], v[20:35]
	ds_read_b64_tr_b16 v[82:83], v69 offset:57344
	ds_read_b64_tr_b16 v[84:85], v2 offset:57344
	s_waitcnt lgkmcnt(0)
	v_mfma_f32_32x32x16_bf16 v[4:19], v[78:81], v[82:85], v[4:19]
	ds_read_b64_tr_b16 v[78:79], v77 offset:28672
	ds_read_b64_tr_b16 v[80:81], v75 offset:28672
	ds_read_b64_tr_b16 v[82:83], v76 offset:61440
	ds_read_b64_tr_b16 v[84:85], v74 offset:61440
	ds_read_b64_tr_b16 v[74:75], v73 offset:61440
	ds_read_b64_tr_b16 v[76:77], v72 offset:61440
	s_waitcnt lgkmcnt(0)
	v_mfma_f32_32x32x16_bf16 v[36:51], v[78:81], v[74:77], v[36:51]
	ds_read_b64_tr_b16 v[72:73], v71 offset:61440
	ds_read_b64_tr_b16 v[74:75], v70 offset:61440
	v_mfma_f32_32x32x16_bf16 v[52:67], v[78:81], v[82:85], v[52:67]
	s_waitcnt lgkmcnt(0)
; #define WG_BAR() do { asm volatile("s_waitcnt vmcnt(0) lgkmcnt(0)" ::: "memory"); __builtin_amdgcn_s_barrier(); asm volatile("" ::: "memory"); } while (0)
; __device__ __forceinline__ int crow(int r, int hi) { return (r & 3) + 8 * (r >> 2) + 4 * hi; }
; __device__ __forceinline__ void retA_unit2(LAS unsigned char* lds, const bf16* proj, const f32x2* rot, float* KV, int uA, int uB, int tid, int lane, int wid) {
;     ...
;     float* kvp = KV + (size_t)u * 16384;
; #pragma unroll
;     for (int k = 0; k < 4; ++k)
; #pragma unroll
;         for (int r = 0; r < 16; ++r) kvp[(32 * db + crow(r, hi)) * 128 + 32 * k + r32] = acc[k][r];
;     WG_BAR();
	v_mfma_f32_32x32x16_bf16 v[20:35], v[78:81], v[72:75], v[20:35]
	ds_read_b64_tr_b16 v[70:71], v69 offset:61440
	ds_read_b64_tr_b16 v[72:73], v2 offset:61440
	v_and_or_b32 v2, v68, 31, s3
	v_lshlrev_b32_e32 v68, 4, v68
	v_and_b32_e32 v68, 0x200, v68
	v_or_b32_e32 v69, v68, v2
	v_lshlrev_b32_e32 v69, 2, v69
	s_nop 2
	global_store_dword v69, v52, s[4:5]
	v_add_lshl_u32 v52, v68, v2, 2
	global_store_dword v52, v53, s[4:5] offset:512
	global_store_dword v52, v54, s[4:5] offset:1024
	global_store_dword v52, v55, s[4:5] offset:1536
	v_or_b32_e32 v53, 0x400, v68
	v_or_b32_e32 v54, v53, v2
	v_lshlrev_b32_e32 v54, 2, v54
	global_store_dword v54, v56, s[4:5]
	v_or_b32_e32 v54, 0x480, v68
	v_or_b32_e32 v55, v54, v2
	v_lshlrev_b32_e32 v55, 2, v55
	global_store_dword v55, v57, s[4:5]
	v_or_b32_e32 v55, 0x500, v68
	v_or_b32_e32 v56, v55, v2
	v_lshlrev_b32_e32 v56, 2, v56
	global_store_dword v56, v58, s[4:5]
	v_or_b32_e32 v56, 0x580, v68
	v_or_b32_e32 v57, v56, v2
	v_lshlrev_b32_e32 v57, 2, v57
	global_store_dword v57, v59, s[4:5]
	v_or_b32_e32 v57, 0x800, v68
	v_or_b32_e32 v58, v57, v2
	v_lshlrev_b32_e32 v58, 2, v58
	global_store_dword v58, v60, s[4:5]
	v_or_b32_e32 v58, 0x880, v68
	v_or_b32_e32 v59, v58, v2
	v_lshlrev_b32_e32 v59, 2, v59
	global_store_dword v59, v61, s[4:5]
	v_or_b32_e32 v59, 0x900, v68
	v_or_b32_e32 v60, v59, v2
	v_lshlrev_b32_e32 v60, 2, v60
	global_store_dword v60, v62, s[4:5]
	v_or_b32_e32 v60, 0x980, v68
	v_or_b32_e32 v61, v60, v2
	v_lshlrev_b32_e32 v61, 2, v61
	global_store_dword v61, v63, s[4:5]
	v_or_b32_e32 v61, 0xc00, v68
	v_or_b32_e32 v62, v61, v2
	v_lshlrev_b32_e32 v62, 2, v62
	global_store_dword v62, v64, s[4:5]
	v_or_b32_e32 v62, 0xc80, v68
	v_or_b32_e32 v63, v62, v2
	v_lshlrev_b32_e32 v63, 2, v63
	global_store_dword v63, v65, s[4:5]
	v_or_b32_e32 v63, 0xd00, v68
	v_or_b32_e32 v64, v63, v2
	v_lshlrev_b32_e32 v64, 2, v64
	global_store_dword v64, v66, s[4:5]
	v_or_b32_e32 v64, 0xd80, v68
	v_or_b32_e32 v65, v64, v2
	v_lshlrev_b32_e32 v65, 2, v65
	global_store_dword v65, v67, s[4:5]
	v_or_b32_e32 v65, 32, v2
	global_store_dword v52, v36, s[4:5] offset:128
	v_add_lshl_u32 v36, v68, v65, 2
	global_store_dword v36, v37, s[4:5] offset:512
	global_store_dword v36, v38, s[4:5] offset:1024
	global_store_dword v36, v39, s[4:5] offset:1536
	v_or_b32_e32 v36, v53, v65
	v_lshlrev_b32_e32 v36, 2, v36
	global_store_dword v36, v40, s[4:5]
	v_or_b32_e32 v36, v54, v65
	v_lshlrev_b32_e32 v36, 2, v36
	global_store_dword v36, v41, s[4:5]
	v_or_b32_e32 v36, v55, v65
	v_lshlrev_b32_e32 v36, 2, v36
	global_store_dword v36, v42, s[4:5]
	v_or_b32_e32 v36, v56, v65
	v_lshlrev_b32_e32 v36, 2, v36
	global_store_dword v36, v43, s[4:5]
	v_or_b32_e32 v36, v57, v65
	v_lshlrev_b32_e32 v36, 2, v36
	global_store_dword v36, v44, s[4:5]
	v_or_b32_e32 v36, v58, v65
	v_lshlrev_b32_e32 v36, 2, v36
	global_store_dword v36, v45, s[4:5]
	v_or_b32_e32 v36, v59, v65
	v_lshlrev_b32_e32 v36, 2, v36
	global_store_dword v36, v46, s[4:5]
	v_or_b32_e32 v36, v60, v65
	v_lshlrev_b32_e32 v36, 2, v36
	global_store_dword v36, v47, s[4:5]
	v_or_b32_e32 v36, v61, v65
	v_lshlrev_b32_e32 v36, 2, v36
	global_store_dword v36, v48, s[4:5]
	v_or_b32_e32 v36, v62, v65
	v_lshlrev_b32_e32 v36, 2, v36
	global_store_dword v36, v49, s[4:5]
	v_or_b32_e32 v36, v63, v65
	v_lshlrev_b32_e32 v36, 2, v36
	global_store_dword v36, v50, s[4:5]
	v_or_b32_e32 v36, v64, v65
	v_lshlrev_b32_e32 v36, 2, v36
	global_store_dword v36, v51, s[4:5]
	v_or_b32_e32 v36, 64, v2
	global_store_dword v52, v20, s[4:5] offset:256
	v_add_lshl_u32 v20, v68, v36, 2
	global_store_dword v20, v21, s[4:5] offset:512
	global_store_dword v20, v22, s[4:5] offset:1024
	global_store_dword v20, v23, s[4:5] offset:1536
	v_or_b32_e32 v20, v53, v36
	v_lshlrev_b32_e32 v20, 2, v20
	global_store_dword v20, v24, s[4:5]
	v_or_b32_e32 v20, v54, v36
	v_lshlrev_b32_e32 v20, 2, v20
	global_store_dword v20, v25, s[4:5]
	v_or_b32_e32 v20, v55, v36
	v_lshlrev_b32_e32 v20, 2, v20
	global_store_dword v20, v26, s[4:5]
	v_or_b32_e32 v20, v56, v36
	v_lshlrev_b32_e32 v20, 2, v20
	global_store_dword v20, v27, s[4:5]
	v_or_b32_e32 v20, v57, v36
	v_lshlrev_b32_e32 v20, 2, v20
	global_store_dword v20, v28, s[4:5]
	v_or_b32_e32 v20, v58, v36
	v_lshlrev_b32_e32 v20, 2, v20
	global_store_dword v20, v29, s[4:5]
	v_or_b32_e32 v20, v59, v36
	v_lshlrev_b32_e32 v20, 2, v20
	global_store_dword v20, v30, s[4:5]
	v_or_b32_e32 v20, v60, v36
	v_lshlrev_b32_e32 v20, 2, v20
	s_waitcnt lgkmcnt(0)
	v_mfma_f32_32x32x16_bf16 v[4:19], v[78:81], v[70:73], v[4:19]
	global_store_dword v20, v31, s[4:5]
	v_or_b32_e32 v20, v61, v36
	v_lshlrev_b32_e32 v20, 2, v20
	global_store_dword v20, v32, s[4:5]
	v_or_b32_e32 v20, v62, v36
	v_lshlrev_b32_e32 v20, 2, v20
	global_store_dword v20, v33, s[4:5]
	v_or_b32_e32 v20, v63, v36
	v_lshlrev_b32_e32 v20, 2, v20
	global_store_dword v20, v34, s[4:5]
	v_or_b32_e32 v20, v64, v36
	v_lshlrev_b32_e32 v20, 2, v20
	v_or_b32_e32 v2, 0x60, v2
	global_store_dword v20, v35, s[4:5]
	global_store_dword v52, v4, s[4:5] offset:384
	v_add_lshl_u32 v4, v68, v2, 2
	global_store_dword v4, v5, s[4:5] offset:512
	global_store_dword v4, v6, s[4:5] offset:1024
	global_store_dword v4, v7, s[4:5] offset:1536
	v_or_b32_e32 v4, v53, v2
	v_lshlrev_b32_e32 v4, 2, v4
	global_store_dword v4, v8, s[4:5]
	v_or_b32_e32 v4, v54, v2
	v_lshlrev_b32_e32 v4, 2, v4
	global_store_dword v4, v9, s[4:5]
	v_or_b32_e32 v4, v55, v2
	v_lshlrev_b32_e32 v4, 2, v4
	global_store_dword v4, v10, s[4:5]
	v_or_b32_e32 v4, v56, v2
	v_lshlrev_b32_e32 v4, 2, v4
	global_store_dword v4, v11, s[4:5]
	v_or_b32_e32 v4, v57, v2
	v_lshlrev_b32_e32 v4, 2, v4
	global_store_dword v4, v12, s[4:5]
	v_or_b32_e32 v4, v58, v2
	v_lshlrev_b32_e32 v4, 2, v4
	global_store_dword v4, v13, s[4:5]
	v_or_b32_e32 v4, v59, v2
	v_lshlrev_b32_e32 v4, 2, v4
	global_store_dword v4, v14, s[4:5]
	v_or_b32_e32 v4, v60, v2
	v_lshlrev_b32_e32 v4, 2, v4
	global_store_dword v4, v15, s[4:5]
	v_or_b32_e32 v4, v61, v2
	v_lshlrev_b32_e32 v4, 2, v4
	global_store_dword v4, v16, s[4:5]
	v_or_b32_e32 v4, v62, v2
	v_lshlrev_b32_e32 v4, 2, v4
	global_store_dword v4, v17, s[4:5]
	v_or_b32_e32 v4, v63, v2
	v_or_b32_e32 v2, v64, v2
	v_lshlrev_b32_e32 v4, 2, v4
	v_lshlrev_b32_e32 v2, 2, v2
	global_store_dword v4, v18, s[4:5]
	global_store_dword v2, v19, s[4:5]
	s_waitcnt vmcnt(0) lgkmcnt(0)
	s_barrier
